# KVB chunk tensor tile-major (GLA-A stores contiguous 512 B, scan loads remapped); without the OG layout change
# speedup vs baseline: 1.0079x; 1.0021x over previous
.LBB0_809:
	v_readlane_b32 s94, v254, 7
	v_readlane_b32 s95, v254, 8
	s_mov_b64 s[6:7], s[94:95]
	s_cmp_le_i32 s6, s20
	s_cselect_b64 s[4:5], -1, 0
	s_cmp_lt_i32 s20, s7
	s_cselect_b64 s[6:7], -1, 0
	v_mbcnt_lo_u32_b32 v2, -1, 0
	v_mbcnt_hi_u32_b32 v2, -1, v2
	s_and_b64 s[46:47], s[4:5], s[6:7]
	v_or_b32_e32 v0, s66, v2
	s_mov_b32 s92, s71
	v_readfirstlane_b32 s2, v0
	s_andn2_b64 vcc, exec, s[46:47]
	s_cbranch_vccnz .LBB0_934
	s_bitcmp0_b32 s92, 3
	s_cbranch_scc1 .LBB0_837
	s_cmpk_gt_i32 s92, 0x47f
	s_cbranch_scc1 .LBB0_836
	s_add_u32 s78, s44, 0xbcf8000
	s_addc_u32 s79, s45, 0
	s_add_u32 s80, s44, 0x64dc8000
	v_and_b32_e32 v4, 48, v2
	v_mov_b32_e32 v5, v97
	s_addc_u32 s81, s45, 0
	v_lshlrev_b32_e32 v1, 2, v0
	s_ashr_i32 s10, s2, 6
	v_lshl_add_u64 v[6:7], s[44:45], 0, v[4:5]
	s_mov_b64 s[2:3], 0x62548000
	v_ashrrev_i32_e32 v91, 7, v0
	v_readlane_b32 s42, v255, 18
	v_add_u32_e32 v90, 0, v1
	v_lshl_add_u64 v[60:61], v[6:7], 0, s[2:3]
	v_and_b32_e32 v6, 0x1fc, v1
	v_mov_b32_e32 v7, v97
	v_add_u32_e32 v92, s42, v1
	v_lshlrev_b32_e32 v1, 13, v91
	v_lshl_add_u64 v[8:9], s[44:45], 0, v[6:7]
	s_mov_b64 s[2:3], 0x1b118000
	v_add3_u32 v93, 0, v1, v6
	v_ashrrev_i32_e32 v66, 3, v0
	v_lshlrev_b32_e32 v1, 4, v2
	s_movk_i32 s13, 0x110
	v_lshl_add_u64 v[64:65], v[8:9], 0, s[2:3]
	v_and_b32_e32 v8, 0x70, v1
	v_mul_lo_u32 v1, v66, s13
	v_add_u32_e32 v7, 0, v1
	s_movk_i32 s6, 0x80
	v_ashrrev_i32_e32 v1, 31, v0
	v_cmp_gt_i32_e64 s[6:7], s6, v0
	v_lshl_add_u64 v[0:1], v[0:1], 2, s[44:45]
	s_mov_b64 s[14:15], 0x6a7c8000
	v_lshl_add_u64 v[68:69], v[0:1], 0, s[14:15]
	s_lshl_b32 s11, s10, 3
	v_lshlrev_b32_e32 v0, 1, v2
	s_and_b32 s11, s11, 0xfffffe0
	v_and_b32_e32 v0, 24, v0
	v_and_b32_e32 v1, 3, v2
	v_and_b32_e32 v56, 15, v2
	v_or3_b32 v0, v1, v0, s11
	s_lshl_b32 s11, s10, 4
	v_and_b32_e32 v3, 63, v2
	v_bfe_u32 v10, v2, 4, 2
	s_lshl_b32 s8, s10, 5
	v_and_or_b32 v2, s11, 48, v56
	s_and_b32 s11, s10, 0x1ffffffc
	s_lshl_b32 s10, s10, 10
	s_ashr_i32 s9, s8, 31
	s_add_i32 s88, s10, 0
	v_or_b32_e32 v58, s8, v56
	v_mov_b32_e32 v59, s9
	s_add_i32 s88, s88, 0x15000
	s_lshl_b64 s[8:9], s[8:9], 1
	v_mul_lo_u32 v0, v0, s13
	s_add_u32 s8, s44, s8
	v_lshlrev_b32_e32 v96, 3, v10
	v_add_u32_e32 v12, 0, v0
	v_or_b32_e32 v0, s11, v10
	s_addc_u32 s9, s45, s9
	v_lshlrev_b32_e32 v10, 3, v0
	v_lshl_add_u64 v[0:1], s[8:9], 0, v[96:97]
	s_mov_b64 s[8:9], 0x1d518000
	v_lshl_add_u64 v[70:71], v[0:1], 0, s[8:9]
	v_lshl_add_u64 v[0:1], s[44:45], 0, v[96:97]
	v_or_b32_e32 v14, 1, v10
	s_mov_b64 s[82:83], 0x65fc8200
	v_cmp_ge_i32_e64 s[14:15], v14, v2
	v_or_b32_e32 v14, 2, v10
	v_lshl_add_u64 v[74:75], v[0:1], 0, s[82:83]
	s_mov_b64 s[82:83], 0x65fc8400
	v_cmp_le_i32_e64 s[16:17], v14, v2
	v_cmp_ge_i32_e64 s[18:19], v14, v2
	v_or_b32_e32 v14, 3, v10
	v_lshl_add_u64 v[76:77], v[0:1], 0, s[82:83]
	s_mov_b64 s[82:83], 0x65fc8600
	v_cmp_le_i32_e64 s[20:21], v14, v2
	v_cmp_ge_i32_e64 s[22:23], v14, v2
	v_or_b32_e32 v14, 4, v10
	v_lshl_add_u64 v[78:79], v[0:1], 0, s[82:83]
	s_mov_b64 s[82:83], 0x65fc8800
	v_readlane_b32 s12, v255, 19
	s_mov_b64 s[8:9], 0x65fc8000
	v_cmp_le_i32_e64 s[24:25], v14, v2
	v_cmp_ge_i32_e64 s[26:27], v14, v2
	v_or_b32_e32 v14, 5, v10
	v_lshl_add_u64 v[80:81], v[0:1], 0, s[82:83]
	s_mov_b64 s[82:83], 0x65fc8a00
	v_lshl_add_u32 v5, v66, 1, s12
	v_mad_u32_u24 v11, v2, s13, 0
	v_lshlrev_b32_e32 v94, 4, v3
	v_add_u32_e32 v3, s12, v4
	v_lshl_add_u64 v[72:73], v[0:1], 0, s[8:9]
	v_cmp_le_i32_e64 s[8:9], v10, v2
	v_cmp_ge_i32_e64 s[10:11], v10, v2
	v_cmp_lt_i32_e64 s[12:13], v10, v2
	v_cmp_le_i32_e64 s[28:29], v14, v2
	v_cmp_ge_i32_e64 s[30:31], v14, v2
	v_or_b32_e32 v14, 6, v10
	v_or_b32_e32 v10, 7, v10
	v_lshl_add_u64 v[82:83], v[0:1], 0, s[82:83]
	s_mov_b64 s[82:83], 0x65fc8c00
	v_lshlrev_b32_e32 v62, 4, v91
	v_lshlrev_b32_e32 v9, 1, v8
	v_lshl_add_u32 v95, v8, 2, 0
	v_mul_u32_u24_e32 v13, 0x90, v8
	v_cmp_le_i32_e64 s[34:35], v14, v2
	v_cmp_ge_i32_e64 s[36:37], v14, v2
	v_cmp_le_i32_e64 s[38:39], v10, v2
	v_cmp_ge_i32_e64 s[40:41], v10, v2
	v_mul_u32_u24_e32 v2, 0x90, v56
	v_lshl_add_u64 v[84:85], v[0:1], 0, s[82:83]
	s_mov_b64 s[82:83], 0x65fc8e00
	v_readlane_b32 s43, v255, 20
	v_mov_b32_e32 v57, v97
	v_ashrrev_i32_e32 v63, 31, v62
	v_cmp_gt_i32_e64 s[2:3], 3, v91
	v_cmp_lt_i32_e64 s[4:5], 0, v91
	v_ashrrev_i32_e32 v67, 31, v66
	v_lshl_add_u32 v98, v66, 9, v95
	v_lshl_add_u64 v[86:87], v[0:1], 0, s[82:83]
	v_and_b32_e32 v88, 0xffffffe0, v58
	v_lshlrev_b32_e32 v88, 8, v88
	v_and_b32_e32 v89, 15, v58
	v_lshl_or_b32 v88, v89, 5, v88
	v_mov_b32_e32 v89, v97
	v_add_u32_e32 v99, s43, v6
	v_add_u32_e32 v100, s42, v6
	v_lshlrev_b32_e32 v96, 1, v8
	v_add_u32_e32 v101, v5, v13
	v_add_u32_e32 v102, v7, v9
	v_add_u32_e32 v103, v11, v4
	v_add_u32_e32 v104, v12, v4
	v_add_u32_e32 v105, v3, v2
	s_branch .LBB0_814
.LBB0_813:
	s_or_b64 exec, exec, s[84:85]
	s_waitcnt lgkmcnt(0)
	s_barrier
	ds_read_b128 v[0:3], v103 offset:32768
	ds_read_b128 v[4:7], v104 offset:50176
	ds_read_b128 v[8:11], v104 offset:51264
	s_waitcnt lgkmcnt(1)
	v_mfma_f32_16x16x32_bf16 v[4:7], v[4:7], v[0:3], 0
	s_lshl_b32 s76, s89, 1
	s_waitcnt lgkmcnt(0)
	v_mfma_f32_16x16x32_bf16 v[0:3], v[8:11], v[0:3], 0
	ds_read_b128 v[8:11], v103 offset:32832
	ds_read_b128 v[12:15], v104 offset:50240
	ds_read_b128 v[16:19], v104 offset:51328
	s_waitcnt lgkmcnt(1)
	v_mfma_f32_16x16x32_bf16 v[4:7], v[12:15], v[8:11], v[4:7]
	s_waitcnt lgkmcnt(0)
	v_mfma_f32_16x16x32_bf16 v[0:3], v[16:19], v[8:11], v[0:3]
	ds_read_b128 v[8:11], v103 offset:32896
	ds_read_b128 v[12:15], v104 offset:50304
	ds_read_b128 v[16:19], v104 offset:51392
	s_waitcnt lgkmcnt(1)
	v_mfma_f32_16x16x32_bf16 v[4:7], v[12:15], v[8:11], v[4:7]
	s_waitcnt lgkmcnt(0)
	v_mfma_f32_16x16x32_bf16 v[0:3], v[16:19], v[8:11], v[0:3]
	ds_read_b128 v[8:11], v103 offset:32960
	ds_read_b128 v[12:15], v104 offset:50368
	ds_read_b128 v[16:19], v104 offset:51456
	s_waitcnt lgkmcnt(1)
	v_mfma_f32_16x16x32_bf16 v[4:7], v[12:15], v[8:11], v[4:7]
	v_add_u32_e32 v14, 0, v94
	s_waitcnt lgkmcnt(0)
	v_mfma_f32_16x16x32_bf16 v[0:3], v[16:19], v[8:11], v[0:3]
	v_cndmask_b32_e64 v8, 0, 1, s[8:9]
	v_cndmask_b32_e64 v9, 0, 1, s[10:11]
	v_cndmask_b32_e64 v8, v9, v8, s[42:43]
	v_and_b32_e32 v8, 1, v8
	v_cmp_eq_u32_e32 vcc, 1, v8
	v_cndmask_b32_e64 v8, 0, 1, s[12:13]
	v_cndmask_b32_e64 v9, 0, 1, s[14:15]
	v_cndmask_b32_e64 v8, v9, v8, s[42:43]
	v_and_b32_e32 v8, 1, v8
	v_cndmask_b32_e32 v4, 0, v4, vcc
	v_cmp_eq_u32_e32 vcc, 1, v8
	v_cndmask_b32_e64 v8, 0, 1, s[16:17]
	v_cndmask_b32_e64 v9, 0, 1, s[18:19]
	v_cndmask_b32_e64 v8, v9, v8, s[42:43]
	v_and_b32_e32 v8, 1, v8
	v_cndmask_b32_e32 v5, 0, v5, vcc
	v_cmp_eq_u32_e32 vcc, 1, v8
	v_cndmask_b32_e64 v8, 0, 1, s[20:21]
	v_cndmask_b32_e64 v9, 0, 1, s[22:23]
	v_cndmask_b32_e64 v8, v9, v8, s[42:43]
	v_and_b32_e32 v8, 1, v8
	v_cndmask_b32_e32 v6, 0, v6, vcc
	v_cmp_eq_u32_e32 vcc, 1, v8
	v_cndmask_b32_e64 v8, 0, 1, s[24:25]
	v_cndmask_b32_e64 v9, 0, 1, s[26:27]
	v_cndmask_b32_e64 v8, v9, v8, s[42:43]
	v_and_b32_e32 v8, 1, v8
	v_cndmask_b32_e32 v7, 0, v7, vcc
	v_cmp_eq_u32_e32 vcc, 1, v8
	v_cndmask_b32_e64 v9, 0, 1, s[30:31]
	s_nop 0
	v_cndmask_b32_e32 v8, 0, v0, vcc
	v_cndmask_b32_e64 v0, 0, 1, s[28:29]
	v_cndmask_b32_e64 v0, v9, v0, s[42:43]
	v_and_b32_e32 v0, 1, v0
	v_cmp_eq_u32_e32 vcc, 1, v0
	v_cndmask_b32_e64 v0, 0, 1, s[34:35]
	s_nop 0
	v_cndmask_b32_e32 v9, 0, v1, vcc
	v_cndmask_b32_e64 v1, 0, 1, s[36:37]
	v_cndmask_b32_e64 v0, v1, v0, s[42:43]
	v_and_b32_e32 v0, 1, v0
	v_cmp_eq_u32_e32 vcc, 1, v0
	v_cndmask_b32_e64 v0, 0, 1, s[38:39]
	v_cndmask_b32_e64 v1, 0, 1, s[40:41]
	v_cndmask_b32_e64 v0, v1, v0, s[42:43]
	v_and_b32_e32 v0, 1, v0
	v_cndmask_b32_e32 v10, 0, v2, vcc
	v_cmp_eq_u32_e32 vcc, 1, v0
	v_cvt_pk_bf16_f32 v0, v4, v5
	v_cvt_pk_bf16_f32 v1, v6, v7
	v_cndmask_b32_e32 v3, 0, v3, vcc
	v_cvt_pk_bf16_f32 v2, v8, v9
	v_cvt_pk_bf16_f32 v3, v10, v3
	v_add_u32_e32 v4, s88, v94
	ds_write_b128 v4, v[0:3]
	v_add_u32_e32 v0, 0x15000, v14
	s_waitcnt lgkmcnt(0)
	s_barrier
	ds_read_b128 v[0:3], v0
	v_lshl_add_u64 v[8:9], s[82:83], 0, v[56:57]
	v_add_u32_e32 v4, 0x16000, v14
	v_lshl_add_u64 v[10:11], v[70:71], 0, s[76:77]
	ds_read_b128 v[4:7], v4
	v_lshlrev_b64 v[8:9], 11, v[8:9]
	v_lshl_add_u64 v[12:13], v[10:11], 0, v[8:9]
	s_waitcnt lgkmcnt(1)
	v_mfma_f32_16x16x32_bf16 v[8:11], v[44:47], v[0:3], 0
	s_lshl_b64 s[42:43], s[92:93], 16
	s_add_i32 s92, s92, s96
	s_cmpk_lt_i32 s92, 0x480
	v_mfma_f32_16x16x32_bf16 v[0:3], v[36:39], v[0:3], 0
	s_waitcnt lgkmcnt(0)
	v_mfma_f32_16x16x32_bf16 v[0:3], v[32:35], v[4:7], v[0:3]
	v_mfma_f32_16x16x32_bf16 v[8:11], v[40:43], v[4:7], v[8:11]
	v_add_u32_e32 v4, 0x16400, v14
	s_nop 5
	v_cvt_pk_bf16_f32 v0, v0, v1
	v_cvt_pk_bf16_f32 v1, v2, v3
	global_store_dwordx2 v[12:13], v[0:1], off offset:32
	v_add_u32_e32 v0, 0x15400, v14
	ds_read_b128 v[0:3], v0
	ds_read_b128 v[4:7], v4
	v_cvt_pk_bf16_f32 v8, v8, v9
	v_cvt_pk_bf16_f32 v9, v10, v11
	global_store_dwordx2 v[12:13], v[8:9], off
	s_waitcnt lgkmcnt(1)
	v_mfma_f32_16x16x32_bf16 v[8:11], v[44:47], v[0:3], 0
	v_mfma_f32_16x16x32_bf16 v[0:3], v[36:39], v[0:3], 0
	s_waitcnt lgkmcnt(0)
	v_mfma_f32_16x16x32_bf16 v[8:11], v[40:43], v[4:7], v[8:11]
	v_mfma_f32_16x16x32_bf16 v[0:3], v[32:35], v[4:7], v[0:3]
	v_add_u32_e32 v4, 0x16800, v14
	s_nop 5
	v_cvt_pk_bf16_f32 v8, v8, v9
	v_cvt_pk_bf16_f32 v9, v10, v11
	v_add_co_u32_e32 v10, vcc, s65, v12
	ds_read_b128 v[4:7], v4
	s_nop 0
	v_addc_co_u32_e32 v11, vcc, 0, v13, vcc
	v_cvt_pk_bf16_f32 v0, v0, v1
	v_cvt_pk_bf16_f32 v1, v2, v3
	global_store_dwordx2 v[10:11], v[0:1], off offset:32
	v_add_u32_e32 v0, 0x15800, v14
	ds_read_b128 v[0:3], v0
	global_store_dwordx2 v[10:11], v[8:9], off
	s_waitcnt lgkmcnt(0)
	v_mfma_f32_16x16x32_bf16 v[8:11], v[44:47], v[0:3], 0
	v_mfma_f32_16x16x32_bf16 v[0:3], v[36:39], v[0:3], 0
	v_mfma_f32_16x16x32_bf16 v[8:11], v[40:43], v[4:7], v[8:11]
	v_mfma_f32_16x16x32_bf16 v[0:3], v[32:35], v[4:7], v[0:3]
	v_add_u32_e32 v4, 0x16c00, v14
	s_nop 5
	v_cvt_pk_bf16_f32 v8, v8, v9
	v_cvt_pk_bf16_f32 v9, v10, v11
	v_add_co_u32_e32 v10, vcc, s49, v12
	ds_read_b128 v[4:7], v4
	s_nop 0
	v_addc_co_u32_e32 v11, vcc, 0, v13, vcc
	v_cvt_pk_bf16_f32 v0, v0, v1
	v_cvt_pk_bf16_f32 v1, v2, v3
	global_store_dwordx2 v[10:11], v[0:1], off offset:32
	v_add_u32_e32 v0, 0x15c00, v14
	ds_read_b128 v[0:3], v0
	global_store_dwordx2 v[10:11], v[8:9], off
	s_waitcnt lgkmcnt(0)
	v_mfma_f32_16x16x32_bf16 v[8:11], v[44:47], v[0:3], 0
	v_mfma_f32_16x16x32_bf16 v[0:3], v[36:39], v[0:3], 0
	v_mfma_f32_16x16x32_bf16 v[8:11], v[40:43], v[4:7], v[8:11]
	v_mfma_f32_16x16x32_bf16 v[0:3], v[32:35], v[4:7], v[0:3]
	s_nop 6
	v_cvt_pk_bf16_f32 v8, v8, v9
	v_cvt_pk_bf16_f32 v9, v10, v11
	v_add_co_u32_e32 v10, vcc, s64, v12
	v_cvt_pk_bf16_f32 v0, v0, v1
	s_nop 0
	v_addc_co_u32_e32 v11, vcc, 0, v13, vcc
	v_cvt_pk_bf16_f32 v1, v2, v3
	global_store_dwordx2 v[10:11], v[8:9], off
	global_store_dwordx2 v[10:11], v[0:1], off offset:32
	ds_read_b128 v[4:7], v105
	ds_read_b128 v[8:11], v105 offset:64
	s_waitcnt lgkmcnt(1)
	v_mfma_f32_16x16x32_bf16 v[0:3], v[4:7], v[44:47], 0
	v_mfma_f32_16x16x32_bf16 v[4:7], v[4:7], v[36:39], 0
	s_waitcnt lgkmcnt(0)
	v_mfma_f32_16x16x32_bf16 v[0:3], v[8:11], v[40:43], v[0:3]
	v_mfma_f32_16x16x32_bf16 v[4:7], v[8:11], v[32:35], v[4:7]
	s_nop 6
	v_cvt_pk_bf16_f32 v12, v0, v1
	v_lshl_add_u64 v[0:1], s[42:43], 0, v[88:89]
	v_cvt_pk_bf16_f32 v13, v2, v3
	v_lshl_add_u64 v[2:3], v[72:73], 0, v[0:1]
	v_or_b32_e32 v0, 0x1000, v0
	v_cvt_pk_bf16_f32 v4, v4, v5
	v_cvt_pk_bf16_f32 v5, v6, v7
	v_lshl_add_u64 v[6:7], v[72:73], 0, v[0:1]
	global_store_dwordx2 v[2:3], v[12:13], off
	global_store_dwordx2 v[6:7], v[4:5], off
	ds_read_b128 v[4:7], v105 offset:2304
	ds_read_b128 v[8:11], v105 offset:2368
	s_waitcnt lgkmcnt(1)
	v_mfma_f32_16x16x32_bf16 v[12:15], v[4:7], v[44:47], 0
	v_mfma_f32_16x16x32_bf16 v[4:7], v[4:7], v[36:39], 0
	s_waitcnt lgkmcnt(0)
	v_mfma_f32_16x16x32_bf16 v[12:15], v[8:11], v[40:43], v[12:15]
	v_mfma_f32_16x16x32_bf16 v[4:7], v[8:11], v[32:35], v[4:7]
	s_nop 6
	v_cvt_pk_bf16_f32 v12, v12, v13
	v_cvt_pk_bf16_f32 v13, v14, v15
	v_cvt_pk_bf16_f32 v4, v4, v5
	v_cvt_pk_bf16_f32 v5, v6, v7
	v_lshl_add_u64 v[6:7], v[74:75], 0, v[0:1]
	global_store_dwordx2 v[2:3], v[12:13], off offset:512
	global_store_dwordx2 v[6:7], v[4:5], off
	ds_read_b128 v[4:7], v105 offset:4608
	ds_read_b128 v[8:11], v105 offset:4672
	s_waitcnt lgkmcnt(1)
	v_mfma_f32_16x16x32_bf16 v[12:15], v[4:7], v[44:47], 0
	v_mfma_f32_16x16x32_bf16 v[4:7], v[4:7], v[36:39], 0
	s_waitcnt lgkmcnt(0)
	v_mfma_f32_16x16x32_bf16 v[12:15], v[8:11], v[40:43], v[12:15]
	v_mfma_f32_16x16x32_bf16 v[4:7], v[8:11], v[32:35], v[4:7]
	s_nop 6
	v_cvt_pk_bf16_f32 v12, v12, v13
	v_cvt_pk_bf16_f32 v13, v14, v15
	v_cvt_pk_bf16_f32 v4, v4, v5
	v_cvt_pk_bf16_f32 v5, v6, v7
	v_lshl_add_u64 v[6:7], v[76:77], 0, v[0:1]
	global_store_dwordx2 v[2:3], v[12:13], off offset:1024
	global_store_dwordx2 v[6:7], v[4:5], off
	ds_read_b128 v[4:7], v105 offset:6912
	ds_read_b128 v[8:11], v105 offset:6976
	s_waitcnt lgkmcnt(1)
	v_mfma_f32_16x16x32_bf16 v[12:15], v[4:7], v[44:47], 0
	v_mfma_f32_16x16x32_bf16 v[4:7], v[4:7], v[36:39], 0
	s_waitcnt lgkmcnt(0)
	v_mfma_f32_16x16x32_bf16 v[12:15], v[8:11], v[40:43], v[12:15]
	v_mfma_f32_16x16x32_bf16 v[4:7], v[8:11], v[32:35], v[4:7]
	s_nop 6
	v_cvt_pk_bf16_f32 v12, v12, v13
	v_cvt_pk_bf16_f32 v13, v14, v15
	v_cvt_pk_bf16_f32 v4, v4, v5
	v_cvt_pk_bf16_f32 v5, v6, v7
	v_lshl_add_u64 v[6:7], v[78:79], 0, v[0:1]
	global_store_dwordx2 v[2:3], v[12:13], off offset:1536
	global_store_dwordx2 v[6:7], v[4:5], off
	ds_read_b128 v[4:7], v105 offset:9216
	ds_read_b128 v[8:11], v105 offset:9280
	s_waitcnt lgkmcnt(1)
	v_mfma_f32_16x16x32_bf16 v[12:15], v[4:7], v[44:47], 0
	v_mfma_f32_16x16x32_bf16 v[4:7], v[4:7], v[36:39], 0
	s_waitcnt lgkmcnt(0)
	v_mfma_f32_16x16x32_bf16 v[12:15], v[8:11], v[40:43], v[12:15]
	v_mfma_f32_16x16x32_bf16 v[4:7], v[8:11], v[32:35], v[4:7]
	s_nop 6
	v_cvt_pk_bf16_f32 v12, v12, v13
	v_cvt_pk_bf16_f32 v13, v14, v15
	v_cvt_pk_bf16_f32 v4, v4, v5
	v_cvt_pk_bf16_f32 v5, v6, v7
	v_lshl_add_u64 v[6:7], v[80:81], 0, v[0:1]
	global_store_dwordx2 v[2:3], v[12:13], off offset:2048
	global_store_dwordx2 v[6:7], v[4:5], off
	ds_read_b128 v[4:7], v105 offset:11520
	ds_read_b128 v[8:11], v105 offset:11584
	s_waitcnt lgkmcnt(1)
	v_mfma_f32_16x16x32_bf16 v[12:15], v[4:7], v[44:47], 0
	v_mfma_f32_16x16x32_bf16 v[4:7], v[4:7], v[36:39], 0
	s_waitcnt lgkmcnt(0)
	v_mfma_f32_16x16x32_bf16 v[12:15], v[8:11], v[40:43], v[12:15]
	v_mfma_f32_16x16x32_bf16 v[4:7], v[8:11], v[32:35], v[4:7]
	s_nop 6
	v_cvt_pk_bf16_f32 v12, v12, v13
	v_cvt_pk_bf16_f32 v13, v14, v15
	v_cvt_pk_bf16_f32 v4, v4, v5
	v_cvt_pk_bf16_f32 v5, v6, v7
	v_lshl_add_u64 v[6:7], v[82:83], 0, v[0:1]
	global_store_dwordx2 v[2:3], v[12:13], off offset:2560
	global_store_dwordx2 v[6:7], v[4:5], off
	ds_read_b128 v[4:7], v105 offset:13824
	ds_read_b128 v[8:11], v105 offset:13888
	s_waitcnt lgkmcnt(1)
	v_mfma_f32_16x16x32_bf16 v[12:15], v[4:7], v[44:47], 0
	v_mfma_f32_16x16x32_bf16 v[4:7], v[4:7], v[36:39], 0
	s_waitcnt lgkmcnt(0)
	v_mfma_f32_16x16x32_bf16 v[12:15], v[8:11], v[40:43], v[12:15]
	v_mfma_f32_16x16x32_bf16 v[4:7], v[8:11], v[32:35], v[4:7]
	s_nop 6
	v_cvt_pk_bf16_f32 v12, v12, v13
	v_cvt_pk_bf16_f32 v13, v14, v15
	v_cvt_pk_bf16_f32 v4, v4, v5
	v_cvt_pk_bf16_f32 v5, v6, v7
	v_lshl_add_u64 v[6:7], v[84:85], 0, v[0:1]
	global_store_dwordx2 v[2:3], v[12:13], off offset:3072
	global_store_dwordx2 v[6:7], v[4:5], off
	ds_read_b128 v[4:7], v105 offset:16128
	ds_read_b128 v[8:11], v105 offset:16192
	s_waitcnt lgkmcnt(1)
	v_mfma_f32_16x16x32_bf16 v[12:15], v[4:7], v[44:47], 0
	v_lshl_add_u64 v[0:1], v[86:87], 0, v[0:1]
	s_waitcnt lgkmcnt(0)
	v_mfma_f32_16x16x32_bf16 v[12:15], v[8:11], v[40:43], v[12:15]
	s_nop 7
	v_cvt_pk_bf16_f32 v12, v12, v13
	v_cvt_pk_bf16_f32 v13, v14, v15
	global_store_dwordx2 v[2:3], v[12:13], off offset:3584
	v_mfma_f32_16x16x32_bf16 v[2:5], v[4:7], v[36:39], 0
	v_mfma_f32_16x16x32_bf16 v[2:5], v[8:11], v[32:35], v[2:5]
	s_nop 7
	v_cvt_pk_bf16_f32 v2, v2, v3
	v_cvt_pk_bf16_f32 v3, v4, v5
	global_store_dwordx2 v[0:1], v[2:3], off
	s_cbranch_scc0 .LBB0_836

.LBB0_907:
	v_mbcnt_lo_u32_b32 v2, -1, 0
	v_mbcnt_hi_u32_b32 v2, -1, v2
	s_mov_b32 s78, s71
	v_or_b32_e32 v0, s66, v2
	s_bitcmp1_b32 s78, 3
	v_readfirstlane_b32 s2, v0
	s_cbranch_scc1 .LBB0_934
	s_cmpk_gt_i32 s78, 0x47f
	s_cbranch_scc1 .LBB0_933
	s_add_u32 s80, s44, 0xbcf8000
	s_addc_u32 s81, s45, 0
	s_add_u32 s82, s44, 0x64dc8000
	v_and_b32_e32 v4, 48, v2
	v_mov_b32_e32 v5, v97
	s_addc_u32 s83, s45, 0
	v_lshlrev_b32_e32 v1, 2, v0
	s_ashr_i32 s10, s2, 6
	v_lshl_add_u64 v[6:7], s[44:45], 0, v[4:5]
	s_mov_b64 s[2:3], 0x62548000
	v_ashrrev_i32_e32 v91, 7, v0
	v_readlane_b32 s42, v255, 18
	v_add_u32_e32 v90, 0, v1
	v_lshl_add_u64 v[60:61], v[6:7], 0, s[2:3]
	v_and_b32_e32 v6, 0x1fc, v1
	v_mov_b32_e32 v7, v97
	v_add_u32_e32 v92, s42, v1
	v_lshlrev_b32_e32 v1, 13, v91
	v_lshl_add_u64 v[8:9], s[44:45], 0, v[6:7]
	s_mov_b64 s[2:3], 0x1b118000
	v_add3_u32 v93, 0, v1, v6
	v_ashrrev_i32_e32 v66, 3, v0
	v_lshlrev_b32_e32 v1, 4, v2
	s_movk_i32 s13, 0x110
	v_lshl_add_u64 v[64:65], v[8:9], 0, s[2:3]
	v_and_b32_e32 v8, 0x70, v1
	v_mul_lo_u32 v1, v66, s13
	v_add_u32_e32 v7, 0, v1
	s_movk_i32 s6, 0x80
	v_ashrrev_i32_e32 v1, 31, v0
	v_cmp_gt_i32_e64 s[6:7], s6, v0
	v_lshl_add_u64 v[0:1], v[0:1], 2, s[44:45]
	s_mov_b64 s[14:15], 0x6a7c8000
	v_lshl_add_u64 v[68:69], v[0:1], 0, s[14:15]
	s_lshl_b32 s11, s10, 3
	v_lshlrev_b32_e32 v0, 1, v2
	s_and_b32 s11, s11, 0xfffffe0
	v_and_b32_e32 v0, 24, v0
	v_and_b32_e32 v1, 3, v2
	v_and_b32_e32 v56, 15, v2
	v_or3_b32 v0, v1, v0, s11
	s_lshl_b32 s11, s10, 4
	v_and_b32_e32 v3, 63, v2
	v_bfe_u32 v10, v2, 4, 2
	s_lshl_b32 s8, s10, 5
	v_and_or_b32 v2, s11, 48, v56
	s_and_b32 s11, s10, 0x1ffffffc
	s_lshl_b32 s10, s10, 10
	s_ashr_i32 s9, s8, 31
	s_add_i32 s90, s10, 0
	v_or_b32_e32 v58, s8, v56
	v_mov_b32_e32 v59, s9
	s_add_i32 s90, s90, 0x15000
	s_lshl_b64 s[8:9], s[8:9], 1
	v_mul_lo_u32 v0, v0, s13
	s_add_u32 s8, s44, s8
	v_lshlrev_b32_e32 v96, 3, v10
	v_add_u32_e32 v12, 0, v0
	v_or_b32_e32 v0, s11, v10
	s_addc_u32 s9, s45, s9
	v_lshlrev_b32_e32 v10, 3, v0
	v_lshl_add_u64 v[0:1], s[8:9], 0, v[96:97]
	s_mov_b64 s[8:9], 0x1d518000
	v_lshl_add_u64 v[70:71], v[0:1], 0, s[8:9]
	v_lshl_add_u64 v[0:1], s[44:45], 0, v[96:97]
	v_or_b32_e32 v14, 1, v10
	s_mov_b64 s[84:85], 0x65fc8200
	v_cmp_ge_i32_e64 s[14:15], v14, v2
	v_or_b32_e32 v14, 2, v10
	v_lshl_add_u64 v[74:75], v[0:1], 0, s[84:85]
	s_mov_b64 s[84:85], 0x65fc8400
	v_cmp_le_i32_e64 s[16:17], v14, v2
	v_cmp_ge_i32_e64 s[18:19], v14, v2
	v_or_b32_e32 v14, 3, v10
	v_lshl_add_u64 v[76:77], v[0:1], 0, s[84:85]
	s_mov_b64 s[84:85], 0x65fc8600
	v_cmp_le_i32_e64 s[20:21], v14, v2
	v_cmp_ge_i32_e64 s[22:23], v14, v2
	v_or_b32_e32 v14, 4, v10
	v_lshl_add_u64 v[78:79], v[0:1], 0, s[84:85]
	s_mov_b64 s[84:85], 0x65fc8800
	v_readlane_b32 s12, v255, 19
	s_mov_b64 s[8:9], 0x65fc8000
	v_cmp_le_i32_e64 s[24:25], v14, v2
	v_cmp_ge_i32_e64 s[26:27], v14, v2
	v_or_b32_e32 v14, 5, v10
	v_lshl_add_u64 v[80:81], v[0:1], 0, s[84:85]
	s_mov_b64 s[84:85], 0x65fc8a00
	v_lshl_add_u32 v5, v66, 1, s12
	v_mad_u32_u24 v11, v2, s13, 0
	v_lshlrev_b32_e32 v94, 4, v3
	v_add_u32_e32 v3, s12, v4
	v_lshl_add_u64 v[72:73], v[0:1], 0, s[8:9]
	v_cmp_le_i32_e64 s[8:9], v10, v2
	v_cmp_ge_i32_e64 s[10:11], v10, v2
	v_cmp_lt_i32_e64 s[12:13], v10, v2
	v_cmp_le_i32_e64 s[28:29], v14, v2
	v_cmp_ge_i32_e64 s[30:31], v14, v2
	v_or_b32_e32 v14, 6, v10
	v_or_b32_e32 v10, 7, v10
	v_lshl_add_u64 v[82:83], v[0:1], 0, s[84:85]
	s_mov_b64 s[84:85], 0x65fc8c00
	v_lshlrev_b32_e32 v62, 4, v91
	v_lshlrev_b32_e32 v9, 1, v8
	v_lshl_add_u32 v95, v8, 2, 0
	v_mul_u32_u24_e32 v13, 0x90, v8
	v_cmp_le_i32_e64 s[34:35], v14, v2
	v_cmp_ge_i32_e64 s[36:37], v14, v2
	v_cmp_le_i32_e64 s[38:39], v10, v2
	v_cmp_ge_i32_e64 s[40:41], v10, v2
	v_mul_u32_u24_e32 v2, 0x90, v56
	v_lshl_add_u64 v[84:85], v[0:1], 0, s[84:85]
	s_mov_b64 s[84:85], 0x65fc8e00
	v_readlane_b32 s43, v255, 20
	v_mov_b32_e32 v57, v97
	v_ashrrev_i32_e32 v63, 31, v62
	v_cmp_gt_i32_e64 s[2:3], 3, v91
	v_cmp_lt_i32_e64 s[4:5], 0, v91
	v_ashrrev_i32_e32 v67, 31, v66
	v_lshl_add_u32 v98, v66, 9, v95
	v_lshl_add_u64 v[86:87], v[0:1], 0, s[84:85]
	v_and_b32_e32 v88, 0xffffffe0, v58
	v_lshlrev_b32_e32 v88, 8, v88
	v_and_b32_e32 v89, 15, v58
	v_lshl_or_b32 v88, v89, 5, v88
	v_mov_b32_e32 v89, v97
	v_add_u32_e32 v99, s43, v6
	v_add_u32_e32 v100, s42, v6
	v_lshlrev_b32_e32 v96, 1, v8
	v_add_u32_e32 v101, v5, v13
	v_add_u32_e32 v102, v7, v9
	v_add_u32_e32 v103, v11, v4
	v_add_u32_e32 v104, v12, v4
	v_add_u32_e32 v105, v3, v2
	s_branch .LBB0_911
.LBB0_910:
	s_or_b64 exec, exec, s[86:87]
	s_waitcnt lgkmcnt(0)
	s_barrier
	ds_read_b128 v[0:3], v103 offset:32768
	ds_read_b128 v[4:7], v104 offset:50176
	ds_read_b128 v[8:11], v104 offset:51264
	s_waitcnt lgkmcnt(1)
	v_mfma_f32_16x16x32_bf16 v[4:7], v[4:7], v[0:3], 0
	s_lshl_b32 s76, s91, 1
	s_waitcnt lgkmcnt(0)
	v_mfma_f32_16x16x32_bf16 v[0:3], v[8:11], v[0:3], 0
	ds_read_b128 v[8:11], v103 offset:32832
	ds_read_b128 v[12:15], v104 offset:50240
	ds_read_b128 v[16:19], v104 offset:51328
	s_waitcnt lgkmcnt(1)
	v_mfma_f32_16x16x32_bf16 v[4:7], v[12:15], v[8:11], v[4:7]
	s_waitcnt lgkmcnt(0)
	v_mfma_f32_16x16x32_bf16 v[0:3], v[16:19], v[8:11], v[0:3]
	ds_read_b128 v[8:11], v103 offset:32896
	ds_read_b128 v[12:15], v104 offset:50304
	ds_read_b128 v[16:19], v104 offset:51392
	s_waitcnt lgkmcnt(1)
	v_mfma_f32_16x16x32_bf16 v[4:7], v[12:15], v[8:11], v[4:7]
	s_waitcnt lgkmcnt(0)
	v_mfma_f32_16x16x32_bf16 v[0:3], v[16:19], v[8:11], v[0:3]
	ds_read_b128 v[8:11], v103 offset:32960
	ds_read_b128 v[12:15], v104 offset:50368
	ds_read_b128 v[16:19], v104 offset:51456
	s_waitcnt lgkmcnt(1)
	v_mfma_f32_16x16x32_bf16 v[4:7], v[12:15], v[8:11], v[4:7]
	v_add_u32_e32 v14, 0, v94
	s_waitcnt lgkmcnt(0)
	v_mfma_f32_16x16x32_bf16 v[0:3], v[16:19], v[8:11], v[0:3]
	v_cndmask_b32_e64 v8, 0, 1, s[8:9]
	v_cndmask_b32_e64 v9, 0, 1, s[10:11]
	v_cndmask_b32_e64 v8, v9, v8, s[42:43]
	v_and_b32_e32 v8, 1, v8
	v_cmp_eq_u32_e32 vcc, 1, v8
	v_cndmask_b32_e64 v8, 0, 1, s[12:13]
	v_cndmask_b32_e64 v9, 0, 1, s[14:15]
	v_cndmask_b32_e64 v8, v9, v8, s[42:43]
	v_and_b32_e32 v8, 1, v8
	v_cndmask_b32_e32 v4, 0, v4, vcc
	v_cmp_eq_u32_e32 vcc, 1, v8
	v_cndmask_b32_e64 v8, 0, 1, s[16:17]
	v_cndmask_b32_e64 v9, 0, 1, s[18:19]
	v_cndmask_b32_e64 v8, v9, v8, s[42:43]
	v_and_b32_e32 v8, 1, v8
	v_cndmask_b32_e32 v5, 0, v5, vcc
	v_cmp_eq_u32_e32 vcc, 1, v8
	v_cndmask_b32_e64 v8, 0, 1, s[20:21]
	v_cndmask_b32_e64 v9, 0, 1, s[22:23]
	v_cndmask_b32_e64 v8, v9, v8, s[42:43]
	v_and_b32_e32 v8, 1, v8
	v_cndmask_b32_e32 v6, 0, v6, vcc
	v_cmp_eq_u32_e32 vcc, 1, v8
	v_cndmask_b32_e64 v8, 0, 1, s[24:25]
	v_cndmask_b32_e64 v9, 0, 1, s[26:27]
	v_cndmask_b32_e64 v8, v9, v8, s[42:43]
	v_and_b32_e32 v8, 1, v8
	v_cndmask_b32_e32 v7, 0, v7, vcc
	v_cmp_eq_u32_e32 vcc, 1, v8
	v_cndmask_b32_e64 v9, 0, 1, s[30:31]
	s_nop 0
	v_cndmask_b32_e32 v8, 0, v0, vcc
	v_cndmask_b32_e64 v0, 0, 1, s[28:29]
	v_cndmask_b32_e64 v0, v9, v0, s[42:43]
	v_and_b32_e32 v0, 1, v0
	v_cmp_eq_u32_e32 vcc, 1, v0
	v_cndmask_b32_e64 v0, 0, 1, s[34:35]
	s_nop 0
	v_cndmask_b32_e32 v9, 0, v1, vcc
	v_cndmask_b32_e64 v1, 0, 1, s[36:37]
	v_cndmask_b32_e64 v0, v1, v0, s[42:43]
	v_and_b32_e32 v0, 1, v0
	v_cmp_eq_u32_e32 vcc, 1, v0
	v_cndmask_b32_e64 v0, 0, 1, s[38:39]
	v_cndmask_b32_e64 v1, 0, 1, s[40:41]
	v_cndmask_b32_e64 v0, v1, v0, s[42:43]
	v_and_b32_e32 v0, 1, v0
	v_cndmask_b32_e32 v10, 0, v2, vcc
	v_cmp_eq_u32_e32 vcc, 1, v0
	v_cvt_pk_bf16_f32 v0, v4, v5
	v_cvt_pk_bf16_f32 v1, v6, v7
	v_cndmask_b32_e32 v3, 0, v3, vcc
	v_cvt_pk_bf16_f32 v2, v8, v9
	v_cvt_pk_bf16_f32 v3, v10, v3
	v_add_u32_e32 v4, s90, v94
	ds_write_b128 v4, v[0:3]
	v_add_u32_e32 v0, 0x15000, v14
	s_waitcnt lgkmcnt(0)
	s_barrier
	ds_read_b128 v[0:3], v0
	v_lshl_add_u64 v[8:9], s[84:85], 0, v[56:57]
	v_add_u32_e32 v4, 0x16000, v14
	v_lshl_add_u64 v[10:11], v[70:71], 0, s[76:77]
	ds_read_b128 v[4:7], v4
	v_lshlrev_b64 v[8:9], 11, v[8:9]
	v_lshl_add_u64 v[12:13], v[10:11], 0, v[8:9]
	s_waitcnt lgkmcnt(1)
	v_mfma_f32_16x16x32_bf16 v[8:11], v[44:47], v[0:3], 0
	s_lshl_b64 s[42:43], s[78:79], 16
	s_add_i32 s78, s78, s96
	s_cmpk_lt_i32 s78, 0x480
	v_mfma_f32_16x16x32_bf16 v[0:3], v[36:39], v[0:3], 0
	s_waitcnt lgkmcnt(0)
	v_mfma_f32_16x16x32_bf16 v[0:3], v[32:35], v[4:7], v[0:3]
	v_mfma_f32_16x16x32_bf16 v[8:11], v[40:43], v[4:7], v[8:11]
	v_add_u32_e32 v4, 0x16400, v14
	s_nop 5
	v_cvt_pk_bf16_f32 v0, v0, v1
	v_cvt_pk_bf16_f32 v1, v2, v3
	global_store_dwordx2 v[12:13], v[0:1], off offset:32
	v_add_u32_e32 v0, 0x15400, v14
	ds_read_b128 v[0:3], v0
	ds_read_b128 v[4:7], v4
	v_cvt_pk_bf16_f32 v8, v8, v9
	v_cvt_pk_bf16_f32 v9, v10, v11
	global_store_dwordx2 v[12:13], v[8:9], off
	s_waitcnt lgkmcnt(1)
	v_mfma_f32_16x16x32_bf16 v[8:11], v[44:47], v[0:3], 0
	v_mfma_f32_16x16x32_bf16 v[0:3], v[36:39], v[0:3], 0
	s_waitcnt lgkmcnt(0)
	v_mfma_f32_16x16x32_bf16 v[8:11], v[40:43], v[4:7], v[8:11]
	v_mfma_f32_16x16x32_bf16 v[0:3], v[32:35], v[4:7], v[0:3]
	v_add_u32_e32 v4, 0x16800, v14
	s_nop 5
	v_cvt_pk_bf16_f32 v8, v8, v9
	v_cvt_pk_bf16_f32 v9, v10, v11
	v_add_co_u32_e32 v10, vcc, s65, v12
	ds_read_b128 v[4:7], v4
	s_nop 0
	v_addc_co_u32_e32 v11, vcc, 0, v13, vcc
	v_cvt_pk_bf16_f32 v0, v0, v1
	v_cvt_pk_bf16_f32 v1, v2, v3
	global_store_dwordx2 v[10:11], v[0:1], off offset:32
	v_add_u32_e32 v0, 0x15800, v14
	ds_read_b128 v[0:3], v0
	global_store_dwordx2 v[10:11], v[8:9], off
	s_waitcnt lgkmcnt(0)
	v_mfma_f32_16x16x32_bf16 v[8:11], v[44:47], v[0:3], 0
	v_mfma_f32_16x16x32_bf16 v[0:3], v[36:39], v[0:3], 0
	v_mfma_f32_16x16x32_bf16 v[8:11], v[40:43], v[4:7], v[8:11]
	v_mfma_f32_16x16x32_bf16 v[0:3], v[32:35], v[4:7], v[0:3]
	v_add_u32_e32 v4, 0x16c00, v14
	s_nop 5
	v_cvt_pk_bf16_f32 v8, v8, v9
	v_cvt_pk_bf16_f32 v9, v10, v11
	v_add_co_u32_e32 v10, vcc, s49, v12
	ds_read_b128 v[4:7], v4
	s_nop 0
	v_addc_co_u32_e32 v11, vcc, 0, v13, vcc
	v_cvt_pk_bf16_f32 v0, v0, v1
	v_cvt_pk_bf16_f32 v1, v2, v3
	global_store_dwordx2 v[10:11], v[0:1], off offset:32
	v_add_u32_e32 v0, 0x15c00, v14
	ds_read_b128 v[0:3], v0
	global_store_dwordx2 v[10:11], v[8:9], off
	s_waitcnt lgkmcnt(0)
	v_mfma_f32_16x16x32_bf16 v[8:11], v[44:47], v[0:3], 0
	v_mfma_f32_16x16x32_bf16 v[0:3], v[36:39], v[0:3], 0
	v_mfma_f32_16x16x32_bf16 v[8:11], v[40:43], v[4:7], v[8:11]
	v_mfma_f32_16x16x32_bf16 v[0:3], v[32:35], v[4:7], v[0:3]
	s_nop 6
	v_cvt_pk_bf16_f32 v8, v8, v9
	v_cvt_pk_bf16_f32 v9, v10, v11
	v_add_co_u32_e32 v10, vcc, s64, v12
	v_cvt_pk_bf16_f32 v0, v0, v1
	s_nop 0
	v_addc_co_u32_e32 v11, vcc, 0, v13, vcc
	v_cvt_pk_bf16_f32 v1, v2, v3
	global_store_dwordx2 v[10:11], v[8:9], off
	global_store_dwordx2 v[10:11], v[0:1], off offset:32
	ds_read_b128 v[4:7], v105
	ds_read_b128 v[8:11], v105 offset:64
	s_waitcnt lgkmcnt(1)
	v_mfma_f32_16x16x32_bf16 v[0:3], v[4:7], v[44:47], 0
	v_mfma_f32_16x16x32_bf16 v[4:7], v[4:7], v[36:39], 0
	s_waitcnt lgkmcnt(0)
	v_mfma_f32_16x16x32_bf16 v[0:3], v[8:11], v[40:43], v[0:3]
	v_mfma_f32_16x16x32_bf16 v[4:7], v[8:11], v[32:35], v[4:7]
	s_nop 6
	v_cvt_pk_bf16_f32 v12, v0, v1
	v_lshl_add_u64 v[0:1], s[42:43], 0, v[88:89]
	v_cvt_pk_bf16_f32 v13, v2, v3
	v_lshl_add_u64 v[2:3], v[72:73], 0, v[0:1]
	v_or_b32_e32 v0, 0x1000, v0
	v_cvt_pk_bf16_f32 v4, v4, v5
	v_cvt_pk_bf16_f32 v5, v6, v7
	v_lshl_add_u64 v[6:7], v[72:73], 0, v[0:1]
	global_store_dwordx2 v[2:3], v[12:13], off
	global_store_dwordx2 v[6:7], v[4:5], off
	ds_read_b128 v[4:7], v105 offset:2304
	ds_read_b128 v[8:11], v105 offset:2368
	s_waitcnt lgkmcnt(1)
	v_mfma_f32_16x16x32_bf16 v[12:15], v[4:7], v[44:47], 0
	v_mfma_f32_16x16x32_bf16 v[4:7], v[4:7], v[36:39], 0
	s_waitcnt lgkmcnt(0)
	v_mfma_f32_16x16x32_bf16 v[12:15], v[8:11], v[40:43], v[12:15]
	v_mfma_f32_16x16x32_bf16 v[4:7], v[8:11], v[32:35], v[4:7]
	s_nop 6
	v_cvt_pk_bf16_f32 v12, v12, v13
	v_cvt_pk_bf16_f32 v13, v14, v15
	v_cvt_pk_bf16_f32 v4, v4, v5
	v_cvt_pk_bf16_f32 v5, v6, v7
	v_lshl_add_u64 v[6:7], v[74:75], 0, v[0:1]
	global_store_dwordx2 v[2:3], v[12:13], off offset:512
	global_store_dwordx2 v[6:7], v[4:5], off
	ds_read_b128 v[4:7], v105 offset:4608
	ds_read_b128 v[8:11], v105 offset:4672
	s_waitcnt lgkmcnt(1)
	v_mfma_f32_16x16x32_bf16 v[12:15], v[4:7], v[44:47], 0
	v_mfma_f32_16x16x32_bf16 v[4:7], v[4:7], v[36:39], 0
	s_waitcnt lgkmcnt(0)
	v_mfma_f32_16x16x32_bf16 v[12:15], v[8:11], v[40:43], v[12:15]
	v_mfma_f32_16x16x32_bf16 v[4:7], v[8:11], v[32:35], v[4:7]
	s_nop 6
	v_cvt_pk_bf16_f32 v12, v12, v13
	v_cvt_pk_bf16_f32 v13, v14, v15
	v_cvt_pk_bf16_f32 v4, v4, v5
	v_cvt_pk_bf16_f32 v5, v6, v7
	v_lshl_add_u64 v[6:7], v[76:77], 0, v[0:1]
	global_store_dwordx2 v[2:3], v[12:13], off offset:1024
	global_store_dwordx2 v[6:7], v[4:5], off
	ds_read_b128 v[4:7], v105 offset:6912
	ds_read_b128 v[8:11], v105 offset:6976
	s_waitcnt lgkmcnt(1)
	v_mfma_f32_16x16x32_bf16 v[12:15], v[4:7], v[44:47], 0
	v_mfma_f32_16x16x32_bf16 v[4:7], v[4:7], v[36:39], 0
	s_waitcnt lgkmcnt(0)
	v_mfma_f32_16x16x32_bf16 v[12:15], v[8:11], v[40:43], v[12:15]
	v_mfma_f32_16x16x32_bf16 v[4:7], v[8:11], v[32:35], v[4:7]
	s_nop 6
	v_cvt_pk_bf16_f32 v12, v12, v13
	v_cvt_pk_bf16_f32 v13, v14, v15
	v_cvt_pk_bf16_f32 v4, v4, v5
	v_cvt_pk_bf16_f32 v5, v6, v7
	v_lshl_add_u64 v[6:7], v[78:79], 0, v[0:1]
	global_store_dwordx2 v[2:3], v[12:13], off offset:1536
	global_store_dwordx2 v[6:7], v[4:5], off
	ds_read_b128 v[4:7], v105 offset:9216
	ds_read_b128 v[8:11], v105 offset:9280
	s_waitcnt lgkmcnt(1)
	v_mfma_f32_16x16x32_bf16 v[12:15], v[4:7], v[44:47], 0
	v_mfma_f32_16x16x32_bf16 v[4:7], v[4:7], v[36:39], 0
	s_waitcnt lgkmcnt(0)
	v_mfma_f32_16x16x32_bf16 v[12:15], v[8:11], v[40:43], v[12:15]
	v_mfma_f32_16x16x32_bf16 v[4:7], v[8:11], v[32:35], v[4:7]
	s_nop 6
	v_cvt_pk_bf16_f32 v12, v12, v13
	v_cvt_pk_bf16_f32 v13, v14, v15
	v_cvt_pk_bf16_f32 v4, v4, v5
	v_cvt_pk_bf16_f32 v5, v6, v7
	v_lshl_add_u64 v[6:7], v[80:81], 0, v[0:1]
	global_store_dwordx2 v[2:3], v[12:13], off offset:2048
	global_store_dwordx2 v[6:7], v[4:5], off
	ds_read_b128 v[4:7], v105 offset:11520
	ds_read_b128 v[8:11], v105 offset:11584
	s_waitcnt lgkmcnt(1)
	v_mfma_f32_16x16x32_bf16 v[12:15], v[4:7], v[44:47], 0
	v_mfma_f32_16x16x32_bf16 v[4:7], v[4:7], v[36:39], 0
	s_waitcnt lgkmcnt(0)
	v_mfma_f32_16x16x32_bf16 v[12:15], v[8:11], v[40:43], v[12:15]
	v_mfma_f32_16x16x32_bf16 v[4:7], v[8:11], v[32:35], v[4:7]
	s_nop 6
	v_cvt_pk_bf16_f32 v12, v12, v13
	v_cvt_pk_bf16_f32 v13, v14, v15
	v_cvt_pk_bf16_f32 v4, v4, v5
	v_cvt_pk_bf16_f32 v5, v6, v7
	v_lshl_add_u64 v[6:7], v[82:83], 0, v[0:1]
	global_store_dwordx2 v[2:3], v[12:13], off offset:2560
	global_store_dwordx2 v[6:7], v[4:5], off
	ds_read_b128 v[4:7], v105 offset:13824
	ds_read_b128 v[8:11], v105 offset:13888
	s_waitcnt lgkmcnt(1)
	v_mfma_f32_16x16x32_bf16 v[12:15], v[4:7], v[44:47], 0
	v_mfma_f32_16x16x32_bf16 v[4:7], v[4:7], v[36:39], 0
	s_waitcnt lgkmcnt(0)
	v_mfma_f32_16x16x32_bf16 v[12:15], v[8:11], v[40:43], v[12:15]
	v_mfma_f32_16x16x32_bf16 v[4:7], v[8:11], v[32:35], v[4:7]
	s_nop 6
	v_cvt_pk_bf16_f32 v12, v12, v13
	v_cvt_pk_bf16_f32 v13, v14, v15
	v_cvt_pk_bf16_f32 v4, v4, v5
	v_cvt_pk_bf16_f32 v5, v6, v7
	v_lshl_add_u64 v[6:7], v[84:85], 0, v[0:1]
	global_store_dwordx2 v[2:3], v[12:13], off offset:3072
	global_store_dwordx2 v[6:7], v[4:5], off
	ds_read_b128 v[4:7], v105 offset:16128
	ds_read_b128 v[8:11], v105 offset:16192
	s_waitcnt lgkmcnt(1)
	v_mfma_f32_16x16x32_bf16 v[12:15], v[4:7], v[44:47], 0
	v_lshl_add_u64 v[0:1], v[86:87], 0, v[0:1]
	s_waitcnt lgkmcnt(0)
	v_mfma_f32_16x16x32_bf16 v[12:15], v[8:11], v[40:43], v[12:15]
	s_nop 7
	v_cvt_pk_bf16_f32 v12, v12, v13
	v_cvt_pk_bf16_f32 v13, v14, v15
	global_store_dwordx2 v[2:3], v[12:13], off offset:3584
	v_mfma_f32_16x16x32_bf16 v[2:5], v[4:7], v[36:39], 0
	v_mfma_f32_16x16x32_bf16 v[2:5], v[8:11], v[32:35], v[2:5]
	s_nop 7
	v_cvt_pk_bf16_f32 v2, v2, v3
	v_cvt_pk_bf16_f32 v3, v4, v5
	global_store_dwordx2 v[0:1], v[2:3], off
	s_cbranch_scc0 .LBB0_933

.LBB0_993:
	v_and_b32_e32 v4, 0x7e, v147
	s_mov_b32 s12, 0x40000
	v_ashrrev_i32_e32 v150, 14, v146
	v_cmp_gt_u32_e32 vcc, s12, v146
	v_lshlrev_b32_e32 v2, 1, v4
	v_lshlrev_b32_e32 v4, 2, v4
	v_mov_b32_e32 v5, v97
	v_mul_i32_i24_e32 v10, 36, v150
	v_and_b32_e32 v0, 0x7f80, v147
	v_lshl_add_u64 v[6:7], s[8:9], 0, v[4:5]
	v_cndmask_b32_e64 v4, 3, 0, vcc
	v_and_b32_e32 v96, 0xe, v147
	v_lshlrev_b32_e32 v96, 1, v96
	v_bfe_u32 v0, v147, 7, 4
	v_lshl_or_b32 v96, v0, 5, v96
	v_bfe_u32 v0, v147, 4, 3
	v_lshl_or_b32 v96, v0, 9, v96
	v_bfe_u32 v0, v147, 11, 4
	v_lshl_or_b32 v96, v0, 12, v96
	v_or_b32_e32 v4, v4, v10
	v_lshl_add_u64 v[0:1], s[4:5], 0, v[96:97]
	v_mov_b32_e32 v3, v97
	v_ashrrev_i32_e32 v5, 31, v4
	v_lshlrev_b64 v[142:143], 16, v[4:5]
	v_lshlrev_b64 v[4:5], 9, v[4:5]
	v_lshl_add_u64 v[8:9], v[0:1], 0, v[142:143]
	v_lshl_add_u64 v[4:5], v[6:7], 0, v[4:5]
	global_load_dword v151, v[8:9], off
	global_load_dwordx2 v[144:145], v[4:5], off
	v_cndmask_b32_e64 v4, 2, 1, vcc
	v_or_b32_e32 v4, v4, v10
	v_ashrrev_i32_e32 v5, 31, v4
	v_lshlrev_b64 v[138:139], 16, v[4:5]
	v_lshlrev_b64 v[4:5], 9, v[4:5]
	v_lshl_add_u64 v[8:9], v[0:1], 0, v[138:139]
	v_lshl_add_u64 v[4:5], v[6:7], 0, v[4:5]
	global_load_dword v152, v[8:9], off
	global_load_dwordx2 v[140:141], v[4:5], off
	v_cndmask_b32_e64 v4, 1, 2, vcc
	v_or_b32_e32 v4, v4, v10
	v_ashrrev_i32_e32 v5, 31, v4
	v_lshlrev_b64 v[134:135], 16, v[4:5]
	v_lshlrev_b64 v[4:5], 9, v[4:5]
	v_lshl_add_u64 v[8:9], v[0:1], 0, v[134:135]
	v_lshl_add_u64 v[4:5], v[6:7], 0, v[4:5]
	global_load_dword v153, v[8:9], off
	global_load_dwordx2 v[136:137], v[4:5], off
	v_cndmask_b32_e64 v4, 0, 3, vcc
	v_or_b32_e32 v4, v4, v10
	v_ashrrev_i32_e32 v5, 31, v4
	v_lshlrev_b64 v[130:131], 16, v[4:5]
	v_lshlrev_b64 v[4:5], 9, v[4:5]
	v_lshl_add_u64 v[8:9], v[0:1], 0, v[130:131]
	v_lshl_add_u64 v[4:5], v[6:7], 0, v[4:5]
	global_load_dword v154, v[8:9], off
	global_load_dwordx2 v[132:133], v[4:5], off
	v_cndmask_b32_e64 v4, 35, 4, vcc
	v_mad_i32_i24 v4, v150, 36, v4
	v_ashrrev_i32_e32 v5, 31, v4
	v_lshlrev_b64 v[126:127], 16, v[4:5]
	v_lshlrev_b64 v[4:5], 9, v[4:5]
	v_lshl_add_u64 v[8:9], v[0:1], 0, v[126:127]
	v_lshl_add_u64 v[4:5], v[6:7], 0, v[4:5]
	global_load_dword v155, v[8:9], off
	global_load_dwordx2 v[128:129], v[4:5], off
	v_cndmask_b32_e64 v4, 34, 5, vcc
	v_mad_i32_i24 v4, v150, 36, v4
	v_ashrrev_i32_e32 v5, 31, v4
	v_lshlrev_b64 v[122:123], 16, v[4:5]
	v_lshlrev_b64 v[4:5], 9, v[4:5]
	v_lshl_add_u64 v[8:9], v[0:1], 0, v[122:123]
	v_lshl_add_u64 v[4:5], v[6:7], 0, v[4:5]
	global_load_dword v156, v[8:9], off
	global_load_dwordx2 v[124:125], v[4:5], off
	v_cndmask_b32_e64 v4, 33, 6, vcc
	v_mad_i32_i24 v4, v150, 36, v4
	v_ashrrev_i32_e32 v5, 31, v4
	v_lshlrev_b64 v[118:119], 16, v[4:5]
	v_lshlrev_b64 v[4:5], 9, v[4:5]
	v_lshl_add_u64 v[8:9], v[0:1], 0, v[118:119]
	v_lshl_add_u64 v[4:5], v[6:7], 0, v[4:5]
	global_load_dword v157, v[8:9], off
	global_load_dwordx2 v[120:121], v[4:5], off
	v_cndmask_b32_e64 v4, 32, 7, vcc
	v_mad_i32_i24 v4, v150, 36, v4
	v_ashrrev_i32_e32 v5, 31, v4
	v_lshlrev_b64 v[114:115], 16, v[4:5]
	v_lshlrev_b64 v[4:5], 9, v[4:5]
	v_lshl_add_u64 v[8:9], v[0:1], 0, v[114:115]
	v_lshl_add_u64 v[4:5], v[6:7], 0, v[4:5]
	global_load_dword v158, v[8:9], off
	global_load_dwordx2 v[116:117], v[4:5], off
	v_cndmask_b32_e64 v4, 31, 8, vcc
	v_mad_i32_i24 v4, v150, 36, v4
	v_ashrrev_i32_e32 v5, 31, v4
	v_lshlrev_b64 v[110:111], 16, v[4:5]
	v_lshlrev_b64 v[4:5], 9, v[4:5]
	v_lshl_add_u64 v[8:9], v[0:1], 0, v[110:111]
	v_lshl_add_u64 v[4:5], v[6:7], 0, v[4:5]
	global_load_dword v159, v[8:9], off
	global_load_dwordx2 v[112:113], v[4:5], off
	v_cndmask_b32_e64 v4, 30, 9, vcc
	v_mad_i32_i24 v4, v150, 36, v4
	v_ashrrev_i32_e32 v5, 31, v4
	v_lshlrev_b64 v[106:107], 16, v[4:5]
	v_lshlrev_b64 v[4:5], 9, v[4:5]
	v_lshl_add_u64 v[8:9], v[0:1], 0, v[106:107]
	v_lshl_add_u64 v[4:5], v[6:7], 0, v[4:5]
	global_load_dword v160, v[8:9], off
	global_load_dwordx2 v[108:109], v[4:5], off
	v_cndmask_b32_e64 v4, 29, 10, vcc
	v_mad_i32_i24 v4, v150, 36, v4
	v_ashrrev_i32_e32 v5, 31, v4
	v_lshlrev_b64 v[102:103], 16, v[4:5]
	v_lshlrev_b64 v[4:5], 9, v[4:5]
	v_lshl_add_u64 v[8:9], v[0:1], 0, v[102:103]
	v_lshl_add_u64 v[4:5], v[6:7], 0, v[4:5]
	global_load_dword v161, v[8:9], off
	global_load_dwordx2 v[104:105], v[4:5], off
	v_cndmask_b32_e64 v4, 28, 11, vcc
	v_mad_i32_i24 v4, v150, 36, v4
	v_ashrrev_i32_e32 v5, 31, v4
	v_lshlrev_b64 v[98:99], 16, v[4:5]
	v_lshlrev_b64 v[4:5], 9, v[4:5]
	v_lshl_add_u64 v[8:9], v[0:1], 0, v[98:99]
	v_lshl_add_u64 v[4:5], v[6:7], 0, v[4:5]
	global_load_dword v162, v[8:9], off
	global_load_dwordx2 v[100:101], v[4:5], off
	v_cndmask_b32_e64 v4, 27, 12, vcc
	v_mad_i32_i24 v4, v150, 36, v4
	v_ashrrev_i32_e32 v5, 31, v4
	v_lshlrev_b64 v[92:93], 16, v[4:5]
	v_lshlrev_b64 v[4:5], 9, v[4:5]
	v_lshl_add_u64 v[8:9], v[0:1], 0, v[92:93]
	v_lshl_add_u64 v[4:5], v[6:7], 0, v[4:5]
	global_load_dword v163, v[8:9], off
	global_load_dwordx2 v[94:95], v[4:5], off
	v_cndmask_b32_e64 v4, 26, 13, vcc
	v_mad_i32_i24 v4, v150, 36, v4
	v_ashrrev_i32_e32 v5, 31, v4
	v_lshlrev_b64 v[88:89], 16, v[4:5]
	v_lshlrev_b64 v[4:5], 9, v[4:5]
	v_lshl_add_u64 v[8:9], v[0:1], 0, v[88:89]
	v_lshl_add_u64 v[4:5], v[6:7], 0, v[4:5]
	global_load_dword v164, v[8:9], off
	global_load_dwordx2 v[90:91], v[4:5], off
	v_cndmask_b32_e64 v4, 25, 14, vcc
	v_mad_i32_i24 v4, v150, 36, v4
	v_ashrrev_i32_e32 v5, 31, v4
	v_lshlrev_b64 v[84:85], 16, v[4:5]
	v_lshlrev_b64 v[4:5], 9, v[4:5]
	v_lshl_add_u64 v[8:9], v[0:1], 0, v[84:85]
	v_lshl_add_u64 v[4:5], v[6:7], 0, v[4:5]
	global_load_dword v165, v[8:9], off
	global_load_dwordx2 v[86:87], v[4:5], off
	v_cndmask_b32_e64 v4, 24, 15, vcc
	v_mad_i32_i24 v4, v150, 36, v4
	v_ashrrev_i32_e32 v5, 31, v4
	v_lshlrev_b64 v[80:81], 16, v[4:5]
	v_lshlrev_b64 v[4:5], 9, v[4:5]
	v_lshl_add_u64 v[8:9], v[0:1], 0, v[80:81]
	v_lshl_add_u64 v[4:5], v[6:7], 0, v[4:5]
	global_load_dword v166, v[8:9], off
	global_load_dwordx2 v[82:83], v[4:5], off
	v_cndmask_b32_e64 v4, 23, 16, vcc
	v_mad_i32_i24 v4, v150, 36, v4
	v_ashrrev_i32_e32 v5, 31, v4
	v_lshlrev_b64 v[76:77], 16, v[4:5]
	v_lshlrev_b64 v[4:5], 9, v[4:5]
	v_lshl_add_u64 v[8:9], v[0:1], 0, v[76:77]
	v_lshl_add_u64 v[4:5], v[6:7], 0, v[4:5]
	global_load_dword v167, v[8:9], off
	global_load_dwordx2 v[78:79], v[4:5], off
	v_cndmask_b32_e64 v4, 22, 17, vcc
	v_mad_i32_i24 v4, v150, 36, v4
	v_ashrrev_i32_e32 v5, 31, v4
	v_lshlrev_b64 v[72:73], 16, v[4:5]
	v_lshlrev_b64 v[4:5], 9, v[4:5]
	v_lshl_add_u64 v[8:9], v[0:1], 0, v[72:73]
	v_lshl_add_u64 v[4:5], v[6:7], 0, v[4:5]
	global_load_dword v168, v[8:9], off
	global_load_dwordx2 v[74:75], v[4:5], off
	v_cndmask_b32_e64 v4, 21, 18, vcc
	v_mad_i32_i24 v4, v150, 36, v4
	v_ashrrev_i32_e32 v5, 31, v4
	v_lshlrev_b64 v[68:69], 16, v[4:5]
	v_lshlrev_b64 v[4:5], 9, v[4:5]
	v_lshl_add_u64 v[8:9], v[0:1], 0, v[68:69]
	v_lshl_add_u64 v[4:5], v[6:7], 0, v[4:5]
	global_load_dword v169, v[8:9], off
	global_load_dwordx2 v[70:71], v[4:5], off
	v_cndmask_b32_e64 v4, 20, 19, vcc
	v_mad_i32_i24 v4, v150, 36, v4
	v_ashrrev_i32_e32 v5, 31, v4
	v_lshlrev_b64 v[64:65], 16, v[4:5]
	v_lshlrev_b64 v[4:5], 9, v[4:5]
	v_lshl_add_u64 v[8:9], v[0:1], 0, v[64:65]
	v_lshl_add_u64 v[4:5], v[6:7], 0, v[4:5]
	global_load_dword v170, v[8:9], off
	global_load_dwordx2 v[66:67], v[4:5], off
	v_cndmask_b32_e64 v4, 19, 20, vcc
	v_mad_i32_i24 v4, v150, 36, v4
	v_ashrrev_i32_e32 v5, 31, v4
	v_lshlrev_b64 v[60:61], 16, v[4:5]
	v_lshlrev_b64 v[4:5], 9, v[4:5]
	v_lshl_add_u64 v[8:9], v[0:1], 0, v[60:61]
	v_lshl_add_u64 v[4:5], v[6:7], 0, v[4:5]
	global_load_dword v171, v[8:9], off
	global_load_dwordx2 v[62:63], v[4:5], off
	v_cndmask_b32_e64 v4, 18, 21, vcc
	v_mad_i32_i24 v4, v150, 36, v4
	v_ashrrev_i32_e32 v5, 31, v4
	v_lshlrev_b64 v[56:57], 16, v[4:5]
	v_lshlrev_b64 v[4:5], 9, v[4:5]
	v_lshl_add_u64 v[8:9], v[0:1], 0, v[56:57]
	v_lshl_add_u64 v[4:5], v[6:7], 0, v[4:5]
	global_load_dword v172, v[8:9], off
	global_load_dwordx2 v[58:59], v[4:5], off
	v_cndmask_b32_e64 v4, 17, 22, vcc
	v_mad_i32_i24 v4, v150, 36, v4
	v_ashrrev_i32_e32 v5, 31, v4
	v_lshlrev_b64 v[52:53], 16, v[4:5]
	v_lshlrev_b64 v[4:5], 9, v[4:5]
	v_lshl_add_u64 v[8:9], v[0:1], 0, v[52:53]
	v_lshl_add_u64 v[4:5], v[6:7], 0, v[4:5]
	global_load_dword v173, v[8:9], off
	global_load_dwordx2 v[54:55], v[4:5], off
	v_cndmask_b32_e64 v4, 16, 23, vcc
	v_mad_i32_i24 v4, v150, 36, v4
	v_ashrrev_i32_e32 v5, 31, v4
	v_lshlrev_b64 v[48:49], 16, v[4:5]
	v_lshlrev_b64 v[4:5], 9, v[4:5]
	v_lshl_add_u64 v[8:9], v[0:1], 0, v[48:49]
	v_lshl_add_u64 v[4:5], v[6:7], 0, v[4:5]
	global_load_dword v174, v[8:9], off
	global_load_dwordx2 v[50:51], v[4:5], off
	v_cndmask_b32_e64 v4, 15, 24, vcc
	v_mad_i32_i24 v4, v150, 36, v4
	v_ashrrev_i32_e32 v5, 31, v4
	v_lshlrev_b64 v[44:45], 16, v[4:5]
	v_lshlrev_b64 v[4:5], 9, v[4:5]
	v_lshl_add_u64 v[8:9], v[0:1], 0, v[44:45]
	v_lshl_add_u64 v[4:5], v[6:7], 0, v[4:5]
	global_load_dword v175, v[8:9], off
	global_load_dwordx2 v[46:47], v[4:5], off
	v_cndmask_b32_e64 v4, 14, 25, vcc
	v_mad_i32_i24 v4, v150, 36, v4
	v_ashrrev_i32_e32 v5, 31, v4
	v_lshlrev_b64 v[40:41], 16, v[4:5]
	v_lshlrev_b64 v[4:5], 9, v[4:5]
	v_lshl_add_u64 v[8:9], v[0:1], 0, v[40:41]
	v_lshl_add_u64 v[4:5], v[6:7], 0, v[4:5]
	global_load_dword v176, v[8:9], off
	global_load_dwordx2 v[42:43], v[4:5], off
	v_cndmask_b32_e64 v4, 13, 26, vcc
	v_mad_i32_i24 v4, v150, 36, v4
	v_ashrrev_i32_e32 v5, 31, v4
	v_lshlrev_b64 v[36:37], 16, v[4:5]
	v_lshlrev_b64 v[4:5], 9, v[4:5]
	v_lshl_add_u64 v[8:9], v[0:1], 0, v[36:37]
	v_lshl_add_u64 v[4:5], v[6:7], 0, v[4:5]
	global_load_dword v177, v[8:9], off
	global_load_dwordx2 v[38:39], v[4:5], off
	v_cndmask_b32_e64 v4, 12, 27, vcc
	v_mad_i32_i24 v4, v150, 36, v4
	v_ashrrev_i32_e32 v5, 31, v4
	v_lshlrev_b64 v[32:33], 16, v[4:5]
	v_lshlrev_b64 v[4:5], 9, v[4:5]
	v_lshl_add_u64 v[8:9], v[0:1], 0, v[32:33]
	v_lshl_add_u64 v[4:5], v[6:7], 0, v[4:5]
	global_load_dword v178, v[8:9], off
	global_load_dwordx2 v[34:35], v[4:5], off
	v_cndmask_b32_e64 v4, 11, 28, vcc
	v_mad_i32_i24 v4, v150, 36, v4
	v_ashrrev_i32_e32 v5, 31, v4
	v_lshlrev_b64 v[28:29], 16, v[4:5]
	v_lshlrev_b64 v[4:5], 9, v[4:5]
	v_lshl_add_u64 v[8:9], v[0:1], 0, v[28:29]
	v_lshl_add_u64 v[4:5], v[6:7], 0, v[4:5]
	global_load_dword v179, v[8:9], off
	global_load_dwordx2 v[30:31], v[4:5], off
	v_cndmask_b32_e64 v4, 10, 29, vcc
	v_mad_i32_i24 v4, v150, 36, v4
	v_ashrrev_i32_e32 v5, 31, v4
	v_lshlrev_b64 v[24:25], 16, v[4:5]
	v_lshlrev_b64 v[4:5], 9, v[4:5]
	v_lshl_add_u64 v[8:9], v[0:1], 0, v[24:25]
	v_lshl_add_u64 v[4:5], v[6:7], 0, v[4:5]
	global_load_dword v180, v[8:9], off
	global_load_dwordx2 v[26:27], v[4:5], off
	v_cndmask_b32_e64 v4, 9, 30, vcc
	v_mad_i32_i24 v4, v150, 36, v4
	v_ashrrev_i32_e32 v5, 31, v4
	v_lshlrev_b64 v[20:21], 16, v[4:5]
	v_lshlrev_b64 v[4:5], 9, v[4:5]
	v_lshl_add_u64 v[8:9], v[0:1], 0, v[20:21]
	v_lshl_add_u64 v[4:5], v[6:7], 0, v[4:5]
	global_load_dword v181, v[8:9], off
	global_load_dwordx2 v[22:23], v[4:5], off
	v_cndmask_b32_e64 v4, 8, 31, vcc
	v_mad_i32_i24 v4, v150, 36, v4
	v_ashrrev_i32_e32 v5, 31, v4
	v_lshlrev_b64 v[16:17], 16, v[4:5]
	v_lshlrev_b64 v[4:5], 9, v[4:5]
	v_lshl_add_u64 v[8:9], v[0:1], 0, v[16:17]
	v_lshl_add_u64 v[4:5], v[6:7], 0, v[4:5]
	global_load_dword v182, v[8:9], off
	global_load_dwordx2 v[18:19], v[4:5], off
	v_cndmask_b32_e64 v4, 7, 32, vcc
	v_mad_i32_i24 v4, v150, 36, v4
	v_ashrrev_i32_e32 v5, 31, v4
	v_lshlrev_b64 v[12:13], 16, v[4:5]
	v_lshlrev_b64 v[4:5], 9, v[4:5]
	v_lshl_add_u64 v[8:9], v[0:1], 0, v[12:13]
	v_lshl_add_u64 v[4:5], v[6:7], 0, v[4:5]
	global_load_dword v183, v[8:9], off
	global_load_dwordx2 v[14:15], v[4:5], off
	v_cndmask_b32_e64 v4, 6, 33, vcc
	v_mad_i32_i24 v4, v150, 36, v4
	v_ashrrev_i32_e32 v5, 31, v4
	v_lshlrev_b64 v[8:9], 16, v[4:5]
	v_lshlrev_b64 v[4:5], 9, v[4:5]
	v_lshl_add_u64 v[10:11], v[0:1], 0, v[8:9]
	v_lshl_add_u64 v[4:5], v[6:7], 0, v[4:5]
	global_load_dword v184, v[10:11], off
	v_add_u32_e32 v146, s97, v146
	global_load_dwordx2 v[10:11], v[4:5], off
	v_cndmask_b32_e64 v4, 5, 34, vcc
	v_mad_i32_i24 v148, v150, 36, v4
	v_ashrrev_i32_e32 v149, 31, v148
	v_lshlrev_b64 v[4:5], 16, v[148:149]
	v_lshl_add_u64 v[0:1], v[0:1], 0, v[4:5]
	global_load_dword v185, v[0:1], off
	v_lshlrev_b64 v[0:1], 9, v[148:149]
	v_and_b32_e32 v2, 0x1e, v147
	v_lshlrev_b32_e32 v2, 1, v2
	v_bfe_u32 v3, v147, 5, 2
	v_lshl_or_b32 v2, v3, 10, v2
	v_bfe_u32 v3, v147, 7, 4
	v_lshl_or_b32 v2, v3, 6, v2
	v_bfe_u32 v3, v147, 11, 4
	v_lshl_or_b32 v2, v3, 12, v2
	v_mov_b32_e32 v3, v97
	v_lshl_add_u64 v[2:3], s[6:7], 0, v[2:3]
	v_lshl_add_u64 v[0:1], v[6:7], 0, v[0:1]
	v_lshl_add_u64 v[142:143], v[2:3], 0, v[142:143]
	s_waitcnt vmcnt(0)
	v_lshlrev_b32_e32 v96, 16, v151
	global_load_dwordx2 v[6:7], v[0:1], off
	v_fmac_f32_e32 v96, 0, v144
	global_store_dword v[142:143], v97, off
	v_and_b32_e32 v142, 0xffff0000, v151
	v_fmac_f32_e32 v142, 0, v145
	v_bfe_u32 v143, v96, 16, 1
	v_add3_u32 v143, v96, v143, s51
	v_bfe_u32 v144, v142, 16, 1
	v_lshrrev_b32_e32 v143, 16, v143
	v_add3_u32 v144, v142, v144, s51
	v_and_or_b32 v143, v144, s48, v143
	v_lshl_add_u64 v[138:139], v[2:3], 0, v[138:139]
	global_store_dword v[138:139], v143, off
	v_lshlrev_b32_e32 v138, 16, v152
	v_fmac_f32_e32 v138, v96, v140
	v_and_b32_e32 v96, 0xffff0000, v152
	v_fmac_f32_e32 v96, v142, v141
	v_bfe_u32 v139, v138, 16, 1
	v_add3_u32 v139, v138, v139, s51
	v_bfe_u32 v140, v96, 16, 1
	v_lshrrev_b32_e32 v139, 16, v139
	v_add3_u32 v140, v96, v140, s51
	v_and_or_b32 v139, v140, s48, v139
	v_lshl_add_u64 v[134:135], v[2:3], 0, v[134:135]
	global_store_dword v[134:135], v139, off
	v_lshlrev_b32_e32 v134, 16, v153
	v_fmac_f32_e32 v134, v138, v136
	v_and_b32_e32 v135, 0xffff0000, v153
	v_fmac_f32_e32 v135, v96, v137
	v_bfe_u32 v96, v134, 16, 1
	v_add3_u32 v96, v134, v96, s51
	v_bfe_u32 v136, v135, 16, 1
	v_lshrrev_b32_e32 v96, 16, v96
	v_add3_u32 v136, v135, v136, s51
	v_and_or_b32 v96, v136, s48, v96
	v_lshl_add_u64 v[130:131], v[2:3], 0, v[130:131]
	global_store_dword v[130:131], v96, off
	v_lshlrev_b32_e32 v96, 16, v154
	s_waitcnt vmcnt(62)
	v_fmac_f32_e32 v96, v134, v132
	v_and_b32_e32 v130, 0xffff0000, v154
	v_fmac_f32_e32 v130, v135, v133
	v_bfe_u32 v131, v96, 16, 1
	v_add3_u32 v131, v96, v131, s51
	v_bfe_u32 v132, v130, 16, 1
	v_lshrrev_b32_e32 v131, 16, v131
	v_add3_u32 v132, v130, v132, s51
	v_and_or_b32 v131, v132, s48, v131
	v_lshl_add_u64 v[126:127], v[2:3], 0, v[126:127]
	global_store_dword v[126:127], v131, off
	v_lshlrev_b32_e32 v126, 16, v155
	v_fmac_f32_e32 v126, v96, v128
	v_and_b32_e32 v96, 0xffff0000, v155
	v_fmac_f32_e32 v96, v130, v129
	v_bfe_u32 v127, v126, 16, 1
	v_add3_u32 v127, v126, v127, s51
	v_bfe_u32 v128, v96, 16, 1
	v_lshrrev_b32_e32 v127, 16, v127
	v_add3_u32 v128, v96, v128, s51
	v_and_or_b32 v127, v128, s48, v127
	v_lshl_add_u64 v[122:123], v[2:3], 0, v[122:123]
	global_store_dword v[122:123], v127, off
	v_lshlrev_b32_e32 v122, 16, v156
	v_fmac_f32_e32 v122, v126, v124
	v_and_b32_e32 v123, 0xffff0000, v156
	v_fmac_f32_e32 v123, v96, v125
	v_bfe_u32 v96, v122, 16, 1
	v_add3_u32 v96, v122, v96, s51
	v_bfe_u32 v124, v123, 16, 1
	v_lshrrev_b32_e32 v96, 16, v96
	v_add3_u32 v124, v123, v124, s51
	v_and_or_b32 v96, v124, s48, v96
	v_lshl_add_u64 v[118:119], v[2:3], 0, v[118:119]
	global_store_dword v[118:119], v96, off
	s_waitcnt vmcnt(62)
	v_lshlrev_b32_e32 v96, 16, v157
	v_fmac_f32_e32 v96, v122, v120
	v_and_b32_e32 v118, 0xffff0000, v157
	v_fmac_f32_e32 v118, v123, v121
	v_bfe_u32 v119, v96, 16, 1
	v_add3_u32 v119, v96, v119, s51
	v_bfe_u32 v120, v118, 16, 1
	v_lshrrev_b32_e32 v119, 16, v119
	v_add3_u32 v120, v118, v120, s51
	v_and_or_b32 v119, v120, s48, v119
	v_lshl_add_u64 v[114:115], v[2:3], 0, v[114:115]
	global_store_dword v[114:115], v119, off
	v_lshlrev_b32_e32 v114, 16, v158
	s_waitcnt vmcnt(62)
	v_fmac_f32_e32 v114, v96, v116
	v_and_b32_e32 v96, 0xffff0000, v158
	v_fmac_f32_e32 v96, v118, v117
	v_bfe_u32 v115, v114, 16, 1
	v_add3_u32 v115, v114, v115, s51
	v_bfe_u32 v116, v96, 16, 1
	v_lshrrev_b32_e32 v115, 16, v115
	v_add3_u32 v116, v96, v116, s51
	v_and_or_b32 v115, v116, s48, v115
	v_lshl_add_u64 v[110:111], v[2:3], 0, v[110:111]
	global_store_dword v[110:111], v115, off
	s_waitcnt vmcnt(62)
	v_lshlrev_b32_e32 v110, 16, v159
	s_waitcnt vmcnt(61)
	v_fmac_f32_e32 v110, v114, v112
	v_and_b32_e32 v111, 0xffff0000, v159
	v_fmac_f32_e32 v111, v96, v113
	v_bfe_u32 v96, v110, 16, 1
	v_add3_u32 v96, v110, v96, s51
	v_bfe_u32 v112, v111, 16, 1
	v_lshrrev_b32_e32 v96, 16, v96
	v_add3_u32 v112, v111, v112, s51
	v_and_or_b32 v96, v112, s48, v96
	v_lshl_add_u64 v[106:107], v[2:3], 0, v[106:107]
	global_store_dword v[106:107], v96, off
	s_waitcnt vmcnt(61)
	v_lshlrev_b32_e32 v96, 16, v160
	s_waitcnt vmcnt(60)
	v_fmac_f32_e32 v96, v110, v108
	v_and_b32_e32 v106, 0xffff0000, v160
	v_fmac_f32_e32 v106, v111, v109
	v_bfe_u32 v107, v96, 16, 1
	v_add3_u32 v107, v96, v107, s51
	v_bfe_u32 v108, v106, 16, 1
	v_lshrrev_b32_e32 v107, 16, v107
	v_add3_u32 v108, v106, v108, s51
	v_and_or_b32 v107, v108, s48, v107
	v_lshl_add_u64 v[102:103], v[2:3], 0, v[102:103]
	global_store_dword v[102:103], v107, off
	s_waitcnt vmcnt(60)
	v_lshlrev_b32_e32 v102, 16, v161
	s_waitcnt vmcnt(59)
	v_fmac_f32_e32 v102, v96, v104
	v_and_b32_e32 v96, 0xffff0000, v161
	v_fmac_f32_e32 v96, v106, v105
	v_bfe_u32 v103, v102, 16, 1
	v_add3_u32 v103, v102, v103, s51
	v_bfe_u32 v104, v96, 16, 1
	v_lshrrev_b32_e32 v103, 16, v103
	v_add3_u32 v104, v96, v104, s51
	v_and_or_b32 v103, v104, s48, v103
	v_lshl_add_u64 v[98:99], v[2:3], 0, v[98:99]
	global_store_dword v[98:99], v103, off
	s_waitcnt vmcnt(59)
	v_lshlrev_b32_e32 v98, 16, v162
	s_waitcnt vmcnt(58)
	v_fmac_f32_e32 v98, v102, v100
	v_and_b32_e32 v99, 0xffff0000, v162
	v_fmac_f32_e32 v99, v96, v101
	v_bfe_u32 v96, v98, 16, 1
	v_add3_u32 v96, v98, v96, s51
	v_bfe_u32 v100, v99, 16, 1
	v_lshrrev_b32_e32 v96, 16, v96
	v_add3_u32 v100, v99, v100, s51
	v_and_or_b32 v96, v100, s48, v96
	v_lshl_add_u64 v[92:93], v[2:3], 0, v[92:93]
	global_store_dword v[92:93], v96, off
	s_waitcnt vmcnt(58)
	v_lshlrev_b32_e32 v92, 16, v163
	s_waitcnt vmcnt(57)
	v_fmac_f32_e32 v92, v98, v94
	v_and_b32_e32 v93, 0xffff0000, v163
	v_fmac_f32_e32 v93, v99, v95
	v_bfe_u32 v94, v92, 16, 1
	v_add3_u32 v94, v92, v94, s51
	v_bfe_u32 v95, v93, 16, 1
	v_lshrrev_b32_e32 v94, 16, v94
	v_add3_u32 v95, v93, v95, s51
	v_and_or_b32 v94, v95, s48, v94
	v_lshl_add_u64 v[88:89], v[2:3], 0, v[88:89]
	global_store_dword v[88:89], v94, off
	s_waitcnt vmcnt(57)
	v_lshlrev_b32_e32 v88, 16, v164
	s_waitcnt vmcnt(56)
	v_fmac_f32_e32 v88, v92, v90
	v_and_b32_e32 v89, 0xffff0000, v164
	v_fmac_f32_e32 v89, v93, v91
	v_bfe_u32 v90, v88, 16, 1
	v_add3_u32 v90, v88, v90, s51
	v_bfe_u32 v91, v89, 16, 1
	v_lshrrev_b32_e32 v90, 16, v90
	v_add3_u32 v91, v89, v91, s51
	v_and_or_b32 v90, v91, s48, v90
	v_lshl_add_u64 v[84:85], v[2:3], 0, v[84:85]
	global_store_dword v[84:85], v90, off
	s_waitcnt vmcnt(56)
	v_lshlrev_b32_e32 v84, 16, v165
	s_waitcnt vmcnt(55)
	v_fmac_f32_e32 v84, v88, v86
	v_and_b32_e32 v85, 0xffff0000, v165
	v_fmac_f32_e32 v85, v89, v87
	v_bfe_u32 v86, v84, 16, 1
	v_add3_u32 v86, v84, v86, s51
	v_bfe_u32 v87, v85, 16, 1
	v_lshrrev_b32_e32 v86, 16, v86
	v_add3_u32 v87, v85, v87, s51
	v_and_or_b32 v86, v87, s48, v86
	v_lshl_add_u64 v[80:81], v[2:3], 0, v[80:81]
	global_store_dword v[80:81], v86, off
	s_waitcnt vmcnt(55)
	v_lshlrev_b32_e32 v80, 16, v166
	s_waitcnt vmcnt(54)
	v_fmac_f32_e32 v80, v84, v82
	v_and_b32_e32 v81, 0xffff0000, v166
	v_fmac_f32_e32 v81, v85, v83
	v_bfe_u32 v82, v80, 16, 1
	v_add3_u32 v82, v80, v82, s51
	v_bfe_u32 v83, v81, 16, 1
	v_lshrrev_b32_e32 v82, 16, v82
	v_add3_u32 v83, v81, v83, s51
	v_and_or_b32 v82, v83, s48, v82
	v_lshl_add_u64 v[76:77], v[2:3], 0, v[76:77]
	global_store_dword v[76:77], v82, off
	s_waitcnt vmcnt(54)
	v_lshlrev_b32_e32 v76, 16, v167
	s_waitcnt vmcnt(53)
	v_fmac_f32_e32 v76, v80, v78
	v_and_b32_e32 v77, 0xffff0000, v167
	v_fmac_f32_e32 v77, v81, v79
	v_bfe_u32 v78, v76, 16, 1
	v_add3_u32 v78, v76, v78, s51
	v_bfe_u32 v79, v77, 16, 1
	v_lshrrev_b32_e32 v78, 16, v78
	v_add3_u32 v79, v77, v79, s51
	v_and_or_b32 v78, v79, s48, v78
	v_lshl_add_u64 v[72:73], v[2:3], 0, v[72:73]
	global_store_dword v[72:73], v78, off
	s_waitcnt vmcnt(53)
	v_lshlrev_b32_e32 v72, 16, v168
	s_waitcnt vmcnt(52)
	v_fmac_f32_e32 v72, v76, v74
	v_and_b32_e32 v73, 0xffff0000, v168
	v_fmac_f32_e32 v73, v77, v75
	v_bfe_u32 v74, v72, 16, 1
	v_add3_u32 v74, v72, v74, s51
	v_bfe_u32 v75, v73, 16, 1
	v_lshrrev_b32_e32 v74, 16, v74
	v_add3_u32 v75, v73, v75, s51
	v_and_or_b32 v74, v75, s48, v74
	v_lshl_add_u64 v[68:69], v[2:3], 0, v[68:69]
	global_store_dword v[68:69], v74, off
	s_waitcnt vmcnt(52)
	v_lshlrev_b32_e32 v68, 16, v169
	s_waitcnt vmcnt(51)
	v_fmac_f32_e32 v68, v72, v70
	v_and_b32_e32 v69, 0xffff0000, v169
	v_fmac_f32_e32 v69, v73, v71
	v_bfe_u32 v70, v68, 16, 1
	v_add3_u32 v70, v68, v70, s51
	v_bfe_u32 v71, v69, 16, 1
	v_lshrrev_b32_e32 v70, 16, v70
	v_add3_u32 v71, v69, v71, s51
	v_and_or_b32 v70, v71, s48, v70
	v_lshl_add_u64 v[64:65], v[2:3], 0, v[64:65]
	global_store_dword v[64:65], v70, off
	s_waitcnt vmcnt(51)
	v_lshlrev_b32_e32 v64, 16, v170
	s_waitcnt vmcnt(50)
	v_fmac_f32_e32 v64, v68, v66
	v_and_b32_e32 v65, 0xffff0000, v170
	v_fmac_f32_e32 v65, v69, v67
	v_bfe_u32 v66, v64, 16, 1
	v_add3_u32 v66, v64, v66, s51
	v_bfe_u32 v67, v65, 16, 1
	v_lshrrev_b32_e32 v66, 16, v66
	v_add3_u32 v67, v65, v67, s51
	v_and_or_b32 v66, v67, s48, v66
	v_lshl_add_u64 v[60:61], v[2:3], 0, v[60:61]
	global_store_dword v[60:61], v66, off
	s_waitcnt vmcnt(50)
	v_lshlrev_b32_e32 v60, 16, v171
	s_waitcnt vmcnt(49)
	v_fmac_f32_e32 v60, v64, v62
	v_and_b32_e32 v61, 0xffff0000, v171
	v_fmac_f32_e32 v61, v65, v63
	v_bfe_u32 v62, v60, 16, 1
	v_add3_u32 v62, v60, v62, s51
	v_bfe_u32 v63, v61, 16, 1
	v_lshrrev_b32_e32 v62, 16, v62
	v_add3_u32 v63, v61, v63, s51
	v_and_or_b32 v62, v63, s48, v62
	v_lshl_add_u64 v[56:57], v[2:3], 0, v[56:57]
	global_store_dword v[56:57], v62, off
	s_waitcnt vmcnt(49)
	v_lshlrev_b32_e32 v56, 16, v172
	s_waitcnt vmcnt(48)
	v_fmac_f32_e32 v56, v60, v58
	v_and_b32_e32 v57, 0xffff0000, v172
	v_fmac_f32_e32 v57, v61, v59
	v_bfe_u32 v58, v56, 16, 1
	v_add3_u32 v58, v56, v58, s51
	v_bfe_u32 v59, v57, 16, 1
	v_lshrrev_b32_e32 v58, 16, v58
	v_add3_u32 v59, v57, v59, s51
	v_and_or_b32 v58, v59, s48, v58
	v_lshl_add_u64 v[52:53], v[2:3], 0, v[52:53]
	global_store_dword v[52:53], v58, off
	s_waitcnt vmcnt(48)
	v_lshlrev_b32_e32 v52, 16, v173
	s_waitcnt vmcnt(47)
	v_fmac_f32_e32 v52, v56, v54
	v_and_b32_e32 v53, 0xffff0000, v173
	v_fmac_f32_e32 v53, v57, v55
	v_bfe_u32 v54, v52, 16, 1
	v_add3_u32 v54, v52, v54, s51
	v_bfe_u32 v55, v53, 16, 1
	v_lshrrev_b32_e32 v54, 16, v54
	v_add3_u32 v55, v53, v55, s51
	v_and_or_b32 v54, v55, s48, v54
	v_lshl_add_u64 v[48:49], v[2:3], 0, v[48:49]
	global_store_dword v[48:49], v54, off
	s_waitcnt vmcnt(47)
	v_lshlrev_b32_e32 v48, 16, v174
	s_waitcnt vmcnt(46)
	v_fmac_f32_e32 v48, v52, v50
	v_and_b32_e32 v49, 0xffff0000, v174
	v_fmac_f32_e32 v49, v53, v51
	v_bfe_u32 v50, v48, 16, 1
	v_add3_u32 v50, v48, v50, s51
	v_bfe_u32 v51, v49, 16, 1
	v_lshrrev_b32_e32 v50, 16, v50
	v_add3_u32 v51, v49, v51, s51
	v_and_or_b32 v50, v51, s48, v50
	v_lshl_add_u64 v[44:45], v[2:3], 0, v[44:45]
	global_store_dword v[44:45], v50, off
	s_waitcnt vmcnt(46)
	v_lshlrev_b32_e32 v44, 16, v175
	s_waitcnt vmcnt(45)
	v_fmac_f32_e32 v44, v48, v46
	v_and_b32_e32 v45, 0xffff0000, v175
	v_fmac_f32_e32 v45, v49, v47
	v_bfe_u32 v46, v44, 16, 1
	v_add3_u32 v46, v44, v46, s51
	v_bfe_u32 v47, v45, 16, 1
	v_lshrrev_b32_e32 v46, 16, v46
	v_add3_u32 v47, v45, v47, s51
	v_and_or_b32 v46, v47, s48, v46
	v_lshl_add_u64 v[40:41], v[2:3], 0, v[40:41]
	global_store_dword v[40:41], v46, off
	s_waitcnt vmcnt(45)
	v_lshlrev_b32_e32 v40, 16, v176
	s_waitcnt vmcnt(44)
	v_fmac_f32_e32 v40, v44, v42
	v_and_b32_e32 v41, 0xffff0000, v176
	v_fmac_f32_e32 v41, v45, v43
	v_bfe_u32 v42, v40, 16, 1
	v_add3_u32 v42, v40, v42, s51
	v_bfe_u32 v43, v41, 16, 1
	v_lshrrev_b32_e32 v42, 16, v42
	v_add3_u32 v43, v41, v43, s51
	v_and_or_b32 v42, v43, s48, v42
	v_lshl_add_u64 v[36:37], v[2:3], 0, v[36:37]
	global_store_dword v[36:37], v42, off
	s_waitcnt vmcnt(44)
	v_lshlrev_b32_e32 v36, 16, v177
	s_waitcnt vmcnt(43)
	v_fmac_f32_e32 v36, v40, v38
	v_and_b32_e32 v37, 0xffff0000, v177
	v_fmac_f32_e32 v37, v41, v39
	v_bfe_u32 v38, v36, 16, 1
	v_add3_u32 v38, v36, v38, s51
	v_bfe_u32 v39, v37, 16, 1
	v_lshrrev_b32_e32 v38, 16, v38
	v_add3_u32 v39, v37, v39, s51
	v_and_or_b32 v38, v39, s48, v38
	v_lshl_add_u64 v[32:33], v[2:3], 0, v[32:33]
	global_store_dword v[32:33], v38, off
	s_waitcnt vmcnt(43)
	v_lshlrev_b32_e32 v32, 16, v178
	s_waitcnt vmcnt(42)
	v_fmac_f32_e32 v32, v36, v34
	v_and_b32_e32 v33, 0xffff0000, v178
	v_fmac_f32_e32 v33, v37, v35
	v_bfe_u32 v34, v32, 16, 1
	v_add3_u32 v34, v32, v34, s51
	v_bfe_u32 v35, v33, 16, 1
	v_lshrrev_b32_e32 v34, 16, v34
	v_add3_u32 v35, v33, v35, s51
	v_and_or_b32 v34, v35, s48, v34
	v_lshl_add_u64 v[28:29], v[2:3], 0, v[28:29]
	global_store_dword v[28:29], v34, off
	s_waitcnt vmcnt(42)
	v_lshlrev_b32_e32 v28, 16, v179
	s_waitcnt vmcnt(41)
	v_fmac_f32_e32 v28, v32, v30
	v_and_b32_e32 v29, 0xffff0000, v179
	v_fmac_f32_e32 v29, v33, v31
	v_bfe_u32 v30, v28, 16, 1
	v_add3_u32 v30, v28, v30, s51
	v_bfe_u32 v31, v29, 16, 1
	v_lshrrev_b32_e32 v30, 16, v30
	v_add3_u32 v31, v29, v31, s51
	v_and_or_b32 v30, v31, s48, v30
	v_lshl_add_u64 v[24:25], v[2:3], 0, v[24:25]
	global_store_dword v[24:25], v30, off
	s_waitcnt vmcnt(41)
	v_lshlrev_b32_e32 v24, 16, v180
	s_waitcnt vmcnt(40)
	v_fmac_f32_e32 v24, v28, v26
	v_and_b32_e32 v25, 0xffff0000, v180
	v_fmac_f32_e32 v25, v29, v27
	v_bfe_u32 v26, v24, 16, 1
	v_add3_u32 v26, v24, v26, s51
	v_bfe_u32 v27, v25, 16, 1
	v_lshrrev_b32_e32 v26, 16, v26
	v_add3_u32 v27, v25, v27, s51
	v_and_or_b32 v26, v27, s48, v26
	v_lshl_add_u64 v[20:21], v[2:3], 0, v[20:21]
	global_store_dword v[20:21], v26, off
	s_waitcnt vmcnt(40)
	v_lshlrev_b32_e32 v20, 16, v181
	s_waitcnt vmcnt(39)
	v_fmac_f32_e32 v20, v24, v22
	v_and_b32_e32 v21, 0xffff0000, v181
	v_fmac_f32_e32 v21, v25, v23
	v_bfe_u32 v22, v20, 16, 1
	v_add3_u32 v22, v20, v22, s51
	v_bfe_u32 v23, v21, 16, 1
	v_lshrrev_b32_e32 v22, 16, v22
	v_add3_u32 v23, v21, v23, s51
	v_and_or_b32 v22, v23, s48, v22
	v_lshl_add_u64 v[16:17], v[2:3], 0, v[16:17]
	global_store_dword v[16:17], v22, off
	s_waitcnt vmcnt(39)
	v_lshlrev_b32_e32 v16, 16, v182
	s_waitcnt vmcnt(38)
	v_fmac_f32_e32 v16, v20, v18
	v_and_b32_e32 v17, 0xffff0000, v182
	v_fmac_f32_e32 v17, v21, v19
	v_bfe_u32 v18, v16, 16, 1
	v_add3_u32 v18, v16, v18, s51
	v_bfe_u32 v19, v17, 16, 1
	v_lshrrev_b32_e32 v18, 16, v18
	v_add3_u32 v19, v17, v19, s51
	v_and_or_b32 v18, v19, s48, v18
	v_lshl_add_u64 v[12:13], v[2:3], 0, v[12:13]
	global_store_dword v[12:13], v18, off
	s_waitcnt vmcnt(38)
	v_lshlrev_b32_e32 v12, 16, v183
	s_waitcnt vmcnt(37)
	v_fmac_f32_e32 v12, v16, v14
	v_and_b32_e32 v13, 0xffff0000, v183
	v_fmac_f32_e32 v13, v17, v15
	v_bfe_u32 v14, v12, 16, 1
	v_add3_u32 v14, v12, v14, s51
	v_bfe_u32 v15, v13, 16, 1
	v_lshrrev_b32_e32 v14, 16, v14
	v_add3_u32 v15, v13, v15, s51
	v_and_or_b32 v14, v15, s48, v14
	v_lshl_add_u64 v[8:9], v[2:3], 0, v[8:9]
	global_store_dword v[8:9], v14, off
	s_waitcnt vmcnt(37)
	v_lshlrev_b32_e32 v8, 16, v184
	s_waitcnt vmcnt(36)
	v_fmac_f32_e32 v8, v12, v10
	v_and_b32_e32 v9, 0xffff0000, v184
	v_fmac_f32_e32 v9, v13, v11
	v_bfe_u32 v10, v8, 16, 1
	v_add3_u32 v10, v8, v10, s51
	v_bfe_u32 v11, v9, 16, 1
	v_lshrrev_b32_e32 v10, 16, v10
	v_add3_u32 v11, v9, v11, s51
	v_and_or_b32 v10, v11, s48, v10
	v_lshl_add_u64 v[4:5], v[2:3], 0, v[4:5]
	global_store_dword v[4:5], v10, off
	s_waitcnt vmcnt(36)
	v_lshlrev_b32_e32 v4, 16, v185
	v_cndmask_b32_e64 v0, 4, 35, vcc
	s_waitcnt vmcnt(0)
	v_fmac_f32_e32 v4, v8, v6
	v_and_b32_e32 v5, 0xffff0000, v185
	v_mad_i32_i24 v0, v150, 36, v0
	v_fmac_f32_e32 v5, v9, v7
	v_bfe_u32 v6, v4, 16, 1
	v_ashrrev_i32_e32 v1, 31, v0
	v_add3_u32 v4, v4, v6, s51
	v_bfe_u32 v6, v5, 16, 1
	s_mov_b32 s12, 0x7ffff
	v_lshlrev_b64 v[0:1], 16, v[0:1]
	v_lshrrev_b32_e32 v4, 16, v4
	v_add3_u32 v5, v5, v6, s51
	v_cmp_lt_i32_e32 vcc, s12, v146
	v_and_or_b32 v4, v5, s48, v4
	v_lshl_add_u64 v[0:1], v[2:3], 0, v[0:1]
	v_add_u32_e32 v147, s13, v147
	s_or_b64 s[10:11], vcc, s[10:11]
	global_store_dword v[0:1], v4, off
	s_andn2_b64 exec, exec, s[10:11]
	s_cbranch_execnz .LBB0_993
